# v2 + setprio 1 moved in front of the pre-MMA barrier, setprio 0 behind the post-MMA barrier, redundant lgkmcnt(0) after barrier dropped (all 7 K-loops)
# speedup vs baseline: 1.0277x; 1.0277x over previous
.LBB0_171:
	s_add_u32 s16, s62, 0x4000
	s_addc_u32 s17, s63, 0
	s_cmp_eq_u32 vcc_hi, 28
	s_cselect_b32 s68, s29, s16
	s_cselect_b32 s69, s15, s17
	s_cselect_b32 s67, s53, vcc_lo
	s_cselect_b32 s66, s55, s61
	s_add_u32 s64, s68, 0x8000
	s_addc_u32 s65, s69, 0
	s_add_i32 s16, 0, 0x10000
	s_add_i32 s17, 0, 0x14000
	v_add_u32_e32 v94, s16, v182
	v_add_u32_e32 v114, s17, v182
	ds_read_b128 v[82:85], v94
	ds_read_b128 v[86:89], v94 offset:1024
	ds_read_b128 v[90:93], v94 offset:2048
	ds_read_b128 v[94:97], v94 offset:3072
	ds_read_b128 v[174:177], v114
	ds_read_b128 v[178:181], v114 offset:1024
	ds_read_b128 v[214:217], v114 offset:2048
	ds_read_b128 v[218:221], v114 offset:3072
	v_lshl_add_u64 v[158:159], s[62:63], 0, v[170:171]
	s_add_i32 m0, s37, 0xc000
	ds_read_b128 v[222:225], v212
	ds_read_b128 v[226:229], v212 offset:1024
	ds_read_b128 v[230:233], v212 offset:2048
	ds_read_b128 v[234:237], v212 offset:3072
	ds_read_b128 v[238:241], v212 offset:4096
	ds_read_b128 v[242:245], v212 offset:5120
	ds_read_b128 v[246:249], v212 offset:6144
	ds_read_b128 v[250:253], v212 offset:7168
	global_load_lds_dwordx4 v[158:159], off
	v_lshl_add_u64 v[158:159], s[62:63], 0, v[172:173]
	s_add_i32 m0, s37, 0xe000
	s_nop 0
	global_load_lds_dwordx4 v[158:159], off
	s_waitcnt vmcnt(8)
	s_waitcnt lgkmcnt(0)
	s_setprio 1
	s_barrier
	v_mfma_f32_16x16x32_bf16 v[144:147], v[82:85], v[222:225], v[144:147]
	v_mfma_f32_16x16x32_bf16 v[140:143], v[90:93], v[222:225], v[140:143]
	v_mfma_f32_16x16x32_bf16 v[128:131], v[82:85], v[230:233], v[128:131]
	v_mfma_f32_16x16x32_bf16 v[124:127], v[90:93], v[230:233], v[124:127]
	v_mfma_f32_16x16x32_bf16 v[110:113], v[82:85], v[238:241], v[110:113]
	v_mfma_f32_16x16x32_bf16 v[106:109], v[90:93], v[238:241], v[106:109]
	v_mfma_f32_16x16x32_bf16 v[78:81], v[82:85], v[246:249], v[78:81]
	v_mfma_f32_16x16x32_bf16 v[74:77], v[90:93], v[246:249], v[74:77]
	v_mfma_f32_16x16x32_bf16 v[144:147], v[86:89], v[226:229], v[144:147]
	v_mfma_f32_16x16x32_bf16 v[140:143], v[94:97], v[226:229], v[140:143]
	v_mfma_f32_16x16x32_bf16 v[128:131], v[86:89], v[234:237], v[128:131]
	v_mfma_f32_16x16x32_bf16 v[124:127], v[94:97], v[234:237], v[124:127]
	v_mfma_f32_16x16x32_bf16 v[110:113], v[86:89], v[242:245], v[110:113]
	v_mfma_f32_16x16x32_bf16 v[106:109], v[94:97], v[242:245], v[106:109]
	v_mfma_f32_16x16x32_bf16 v[78:81], v[86:89], v[250:253], v[78:81]
	v_mfma_f32_16x16x32_bf16 v[74:77], v[94:97], v[250:253], v[74:77]
	s_setprio 0
	s_setprio 1
	v_mfma_f32_16x16x32_bf16 v[136:139], v[174:177], v[222:225], v[136:139]
	v_mfma_f32_16x16x32_bf16 v[132:135], v[214:217], v[222:225], v[132:135]
	v_mfma_f32_16x16x32_bf16 v[120:123], v[174:177], v[230:233], v[120:123]
	v_mfma_f32_16x16x32_bf16 v[116:119], v[214:217], v[230:233], v[116:119]
	v_mfma_f32_16x16x32_bf16 v[102:105], v[174:177], v[238:241], v[102:105]
	v_mfma_f32_16x16x32_bf16 v[98:101], v[214:217], v[238:241], v[98:101]
	v_mfma_f32_16x16x32_bf16 v[70:73], v[174:177], v[246:249], v[70:73]
	v_mfma_f32_16x16x32_bf16 v[66:69], v[214:217], v[246:249], v[66:69]
	v_mfma_f32_16x16x32_bf16 v[136:139], v[178:181], v[226:229], v[136:139]
	v_mfma_f32_16x16x32_bf16 v[132:135], v[218:221], v[226:229], v[132:135]
	v_mfma_f32_16x16x32_bf16 v[120:123], v[178:181], v[234:237], v[120:123]
	v_mfma_f32_16x16x32_bf16 v[116:119], v[218:221], v[234:237], v[116:119]
	v_mfma_f32_16x16x32_bf16 v[102:105], v[178:181], v[242:245], v[102:105]
	v_mfma_f32_16x16x32_bf16 v[98:101], v[218:221], v[242:245], v[98:101]
	v_mfma_f32_16x16x32_bf16 v[70:73], v[178:181], v[250:253], v[70:73]
	v_mfma_f32_16x16x32_bf16 v[66:69], v[218:221], v[250:253], v[66:69]
	s_barrier
	s_setprio 0
	s_add_i32 s16, s16, s9
	v_lshl_add_u64 v[158:159], s[66:67], 0, v[150:151]
	s_mov_b32 m0, s16
	ds_read_b128 v[222:225], v212 offset:16384
	ds_read_b128 v[226:229], v212 offset:17408
	ds_read_b128 v[230:233], v212 offset:18432
	ds_read_b128 v[234:237], v212 offset:19456
	ds_read_b128 v[238:241], v212 offset:20480
	ds_read_b128 v[242:245], v212 offset:21504
	ds_read_b128 v[246:249], v212 offset:22528
	ds_read_b128 v[250:253], v212 offset:23552
	global_load_lds_dwordx4 v[158:159], off
	s_add_i32 m0, s16, 0x2000
	s_add_u32 s26, s66, 0x1000
	v_lshl_add_u64 v[158:159], s[66:67], 0, v[154:155]
	s_addc_u32 s27, s67, 0
	s_add_i32 s16, s17, s9
	global_load_lds_dwordx4 v[158:159], off
	v_lshl_add_u64 v[158:159], s[26:27], 0, v[150:151]
	s_mov_b32 m0, s16
	s_nop 0
	global_load_lds_dwordx4 v[158:159], off
	v_lshl_add_u64 v[158:159], s[26:27], 0, v[154:155]
	s_add_i32 m0, s16, 0x2000
	s_nop 0
	global_load_lds_dwordx4 v[158:159], off
	v_lshl_add_u64 v[158:159], s[68:69], 0, v[148:149]
	s_mov_b32 m0, s37
	s_nop 0
	global_load_lds_dwordx4 v[158:159], off
	v_lshl_add_u64 v[158:159], s[68:69], 0, v[152:153]
	s_mov_b32 m0, s70
	s_nop 0
	global_load_lds_dwordx4 v[158:159], off
	s_waitcnt vmcnt(8)
	s_waitcnt lgkmcnt(0)
	s_setprio 1
	s_barrier
	v_mfma_f32_16x16x32_bf16 v[62:65], v[82:85], v[222:225], v[62:65]
	v_mfma_f32_16x16x32_bf16 v[58:61], v[90:93], v[222:225], v[58:61]
	v_mfma_f32_16x16x32_bf16 v[46:49], v[82:85], v[230:233], v[46:49]
	v_mfma_f32_16x16x32_bf16 v[42:45], v[90:93], v[230:233], v[42:45]
	v_mfma_f32_16x16x32_bf16 v[30:33], v[82:85], v[238:241], v[30:33]
	v_mfma_f32_16x16x32_bf16 v[26:29], v[90:93], v[238:241], v[26:29]
	v_mfma_f32_16x16x32_bf16 v[14:17], v[82:85], v[246:249], v[14:17]
	v_mfma_f32_16x16x32_bf16 v[10:13], v[90:93], v[246:249], v[10:13]
	v_mfma_f32_16x16x32_bf16 v[62:65], v[86:89], v[226:229], v[62:65]
	v_mfma_f32_16x16x32_bf16 v[58:61], v[94:97], v[226:229], v[58:61]
	v_mfma_f32_16x16x32_bf16 v[46:49], v[86:89], v[234:237], v[46:49]
	v_mfma_f32_16x16x32_bf16 v[42:45], v[94:97], v[234:237], v[42:45]
	v_mfma_f32_16x16x32_bf16 v[30:33], v[86:89], v[242:245], v[30:33]
	v_mfma_f32_16x16x32_bf16 v[26:29], v[94:97], v[242:245], v[26:29]
	v_mfma_f32_16x16x32_bf16 v[14:17], v[86:89], v[250:253], v[14:17]
	v_mfma_f32_16x16x32_bf16 v[10:13], v[94:97], v[250:253], v[10:13]
	s_setprio 0
	s_setprio 1
	v_mfma_f32_16x16x32_bf16 v[54:57], v[174:177], v[222:225], v[54:57]
	v_mfma_f32_16x16x32_bf16 v[50:53], v[214:217], v[222:225], v[50:53]
	v_mfma_f32_16x16x32_bf16 v[38:41], v[174:177], v[230:233], v[38:41]
	v_mfma_f32_16x16x32_bf16 v[34:37], v[214:217], v[230:233], v[34:37]
	v_mfma_f32_16x16x32_bf16 v[22:25], v[174:177], v[238:241], v[22:25]
	v_mfma_f32_16x16x32_bf16 v[18:21], v[214:217], v[238:241], v[18:21]
	v_mfma_f32_16x16x32_bf16 v[6:9], v[174:177], v[246:249], v[6:9]
	v_mfma_f32_16x16x32_bf16 v[2:5], v[214:217], v[246:249], v[2:5]
	v_mfma_f32_16x16x32_bf16 v[54:57], v[178:181], v[226:229], v[54:57]
	v_mfma_f32_16x16x32_bf16 v[50:53], v[218:221], v[226:229], v[50:53]
	v_mfma_f32_16x16x32_bf16 v[38:41], v[178:181], v[234:237], v[38:41]
	v_mfma_f32_16x16x32_bf16 v[34:37], v[218:221], v[234:237], v[34:37]
	v_mfma_f32_16x16x32_bf16 v[22:25], v[178:181], v[242:245], v[22:25]
	v_mfma_f32_16x16x32_bf16 v[18:21], v[218:221], v[242:245], v[18:21]
	v_mfma_f32_16x16x32_bf16 v[6:9], v[178:181], v[250:253], v[6:9]
	v_mfma_f32_16x16x32_bf16 v[2:5], v[218:221], v[250:253], v[2:5]
	s_barrier
	s_setprio 0
	s_add_i32 s16, 0, 0x18000
	s_add_i32 s17, 0, 0x1c000
	v_add_u32_e32 v94, s16, v182
	v_add_u32_e32 v114, s17, v182
	ds_read_b128 v[82:85], v94
	ds_read_b128 v[86:89], v94 offset:1024
	ds_read_b128 v[90:93], v94 offset:2048
	ds_read_b128 v[94:97], v94 offset:3072
	ds_read_b128 v[174:177], v114
	ds_read_b128 v[178:181], v114 offset:1024
	ds_read_b128 v[214:217], v114 offset:2048
	ds_read_b128 v[218:221], v114 offset:3072
	s_add_u32 s26, s68, 0x4000
	s_addc_u32 s27, s69, 0
	s_mov_b32 m0, s71
	v_lshl_add_u64 v[158:159], s[26:27], 0, v[148:149]
	ds_read_b128 v[222:225], v212 offset:32768
	ds_read_b128 v[226:229], v212 offset:33792
	ds_read_b128 v[230:233], v212 offset:34816
	ds_read_b128 v[234:237], v212 offset:35840
	ds_read_b128 v[238:241], v212 offset:36864
	ds_read_b128 v[242:245], v212 offset:37888
	ds_read_b128 v[246:249], v212 offset:38912
	ds_read_b128 v[250:253], v212 offset:39936
	global_load_lds_dwordx4 v[158:159], off
	v_lshl_add_u64 v[158:159], s[26:27], 0, v[152:153]
	s_mov_b32 m0, s74
	s_nop 0
	global_load_lds_dwordx4 v[158:159], off
	s_waitcnt vmcnt(8)
	s_waitcnt lgkmcnt(0)
	s_setprio 1
	s_barrier
	v_mfma_f32_16x16x32_bf16 v[144:147], v[82:85], v[222:225], v[144:147]
	v_mfma_f32_16x16x32_bf16 v[140:143], v[90:93], v[222:225], v[140:143]
	v_mfma_f32_16x16x32_bf16 v[128:131], v[82:85], v[230:233], v[128:131]
	v_mfma_f32_16x16x32_bf16 v[124:127], v[90:93], v[230:233], v[124:127]
	v_mfma_f32_16x16x32_bf16 v[110:113], v[82:85], v[238:241], v[110:113]
	v_mfma_f32_16x16x32_bf16 v[106:109], v[90:93], v[238:241], v[106:109]
	v_mfma_f32_16x16x32_bf16 v[78:81], v[82:85], v[246:249], v[78:81]
	v_mfma_f32_16x16x32_bf16 v[74:77], v[90:93], v[246:249], v[74:77]
	v_mfma_f32_16x16x32_bf16 v[144:147], v[86:89], v[226:229], v[144:147]
	v_mfma_f32_16x16x32_bf16 v[140:143], v[94:97], v[226:229], v[140:143]
	v_mfma_f32_16x16x32_bf16 v[128:131], v[86:89], v[234:237], v[128:131]
	v_mfma_f32_16x16x32_bf16 v[124:127], v[94:97], v[234:237], v[124:127]
	v_mfma_f32_16x16x32_bf16 v[110:113], v[86:89], v[242:245], v[110:113]
	v_mfma_f32_16x16x32_bf16 v[106:109], v[94:97], v[242:245], v[106:109]
	v_mfma_f32_16x16x32_bf16 v[78:81], v[86:89], v[250:253], v[78:81]
	v_mfma_f32_16x16x32_bf16 v[74:77], v[94:97], v[250:253], v[74:77]
	s_setprio 0
	s_setprio 1
	v_mfma_f32_16x16x32_bf16 v[136:139], v[174:177], v[222:225], v[136:139]
	v_mfma_f32_16x16x32_bf16 v[132:135], v[214:217], v[222:225], v[132:135]
	v_mfma_f32_16x16x32_bf16 v[120:123], v[174:177], v[230:233], v[120:123]
	v_mfma_f32_16x16x32_bf16 v[116:119], v[214:217], v[230:233], v[116:119]
	v_mfma_f32_16x16x32_bf16 v[102:105], v[174:177], v[238:241], v[102:105]
	v_mfma_f32_16x16x32_bf16 v[98:101], v[214:217], v[238:241], v[98:101]
	v_mfma_f32_16x16x32_bf16 v[70:73], v[174:177], v[246:249], v[70:73]
	v_mfma_f32_16x16x32_bf16 v[66:69], v[214:217], v[246:249], v[66:69]
	v_mfma_f32_16x16x32_bf16 v[136:139], v[178:181], v[226:229], v[136:139]
	v_mfma_f32_16x16x32_bf16 v[132:135], v[218:221], v[226:229], v[132:135]
	v_mfma_f32_16x16x32_bf16 v[120:123], v[178:181], v[234:237], v[120:123]
	v_mfma_f32_16x16x32_bf16 v[116:119], v[218:221], v[234:237], v[116:119]
	v_mfma_f32_16x16x32_bf16 v[102:105], v[178:181], v[242:245], v[102:105]
	v_mfma_f32_16x16x32_bf16 v[98:101], v[218:221], v[242:245], v[98:101]
	v_mfma_f32_16x16x32_bf16 v[70:73], v[178:181], v[250:253], v[70:73]
	v_mfma_f32_16x16x32_bf16 v[66:69], v[218:221], v[250:253], v[66:69]
	s_barrier
	s_setprio 0
	s_add_u32 s26, s66, 0x8000
	s_addc_u32 s27, s67, 0
	s_add_i32 s16, s16, s9
	v_lshl_add_u64 v[158:159], s[26:27], 0, v[150:151]
	s_mov_b32 m0, s16
	ds_read_b128 v[222:225], v212 offset:49152
	ds_read_b128 v[226:229], v212 offset:50176
	ds_read_b128 v[230:233], v212 offset:51200
	ds_read_b128 v[234:237], v212 offset:52224
	ds_read_b128 v[238:241], v212 offset:53248
	ds_read_b128 v[242:245], v212 offset:54272
	ds_read_b128 v[246:249], v212 offset:55296
	ds_read_b128 v[250:253], v212 offset:56320
	global_load_lds_dwordx4 v[158:159], off
	s_add_i32 m0, s16, 0x2000
	v_lshl_add_u64 v[158:159], s[26:27], 0, v[154:155]
	s_add_u32 s26, s66, 0x9000
	s_addc_u32 s27, s67, 0
	s_add_i32 s16, s17, s9
	global_load_lds_dwordx4 v[158:159], off
	v_lshl_add_u64 v[158:159], s[26:27], 0, v[150:151]
	s_mov_b32 m0, s16
	s_nop 0
	global_load_lds_dwordx4 v[158:159], off
	v_lshl_add_u64 v[158:159], s[26:27], 0, v[154:155]
	s_add_i32 m0, s16, 0x2000
	s_nop 0
	global_load_lds_dwordx4 v[158:159], off
	v_lshl_add_u64 v[158:159], s[64:65], 0, v[148:149]
	s_mov_b32 m0, s86
	s_nop 0
	global_load_lds_dwordx4 v[158:159], off
	v_lshl_add_u64 v[158:159], s[64:65], 0, v[152:153]
	s_mov_b32 m0, s87
	s_nop 0
	global_load_lds_dwordx4 v[158:159], off
	s_waitcnt vmcnt(8)
	s_waitcnt lgkmcnt(0)
	s_setprio 1
	s_barrier
	v_mfma_f32_16x16x32_bf16 v[62:65], v[82:85], v[222:225], v[62:65]
	v_mfma_f32_16x16x32_bf16 v[58:61], v[90:93], v[222:225], v[58:61]
	v_mfma_f32_16x16x32_bf16 v[46:49], v[82:85], v[230:233], v[46:49]
	v_mfma_f32_16x16x32_bf16 v[42:45], v[90:93], v[230:233], v[42:45]
	v_mfma_f32_16x16x32_bf16 v[30:33], v[82:85], v[238:241], v[30:33]
	v_mfma_f32_16x16x32_bf16 v[26:29], v[90:93], v[238:241], v[26:29]
	v_mfma_f32_16x16x32_bf16 v[14:17], v[82:85], v[246:249], v[14:17]
	v_mfma_f32_16x16x32_bf16 v[10:13], v[90:93], v[246:249], v[10:13]
	v_mfma_f32_16x16x32_bf16 v[62:65], v[86:89], v[226:229], v[62:65]
	v_mfma_f32_16x16x32_bf16 v[58:61], v[94:97], v[226:229], v[58:61]
	v_mfma_f32_16x16x32_bf16 v[46:49], v[86:89], v[234:237], v[46:49]
	v_mfma_f32_16x16x32_bf16 v[42:45], v[94:97], v[234:237], v[42:45]
	v_mfma_f32_16x16x32_bf16 v[30:33], v[86:89], v[242:245], v[30:33]
	v_mfma_f32_16x16x32_bf16 v[26:29], v[94:97], v[242:245], v[26:29]
	v_mfma_f32_16x16x32_bf16 v[14:17], v[86:89], v[250:253], v[14:17]
	v_mfma_f32_16x16x32_bf16 v[10:13], v[94:97], v[250:253], v[10:13]
	s_setprio 0
	s_setprio 1
	v_mfma_f32_16x16x32_bf16 v[54:57], v[174:177], v[222:225], v[54:57]
	v_mfma_f32_16x16x32_bf16 v[50:53], v[214:217], v[222:225], v[50:53]
	v_mfma_f32_16x16x32_bf16 v[38:41], v[174:177], v[230:233], v[38:41]
	v_mfma_f32_16x16x32_bf16 v[34:37], v[214:217], v[230:233], v[34:37]
	v_mfma_f32_16x16x32_bf16 v[22:25], v[174:177], v[238:241], v[22:25]
	v_mfma_f32_16x16x32_bf16 v[18:21], v[214:217], v[238:241], v[18:21]
	v_mfma_f32_16x16x32_bf16 v[6:9], v[174:177], v[246:249], v[6:9]
	v_mfma_f32_16x16x32_bf16 v[2:5], v[214:217], v[246:249], v[2:5]
	v_mfma_f32_16x16x32_bf16 v[54:57], v[178:181], v[226:229], v[54:57]
	v_mfma_f32_16x16x32_bf16 v[50:53], v[218:221], v[226:229], v[50:53]
	v_mfma_f32_16x16x32_bf16 v[38:41], v[178:181], v[234:237], v[38:41]
	v_mfma_f32_16x16x32_bf16 v[34:37], v[218:221], v[234:237], v[34:37]
	v_mfma_f32_16x16x32_bf16 v[22:25], v[178:181], v[242:245], v[22:25]
	v_mfma_f32_16x16x32_bf16 v[18:21], v[218:221], v[242:245], v[18:21]
	v_mfma_f32_16x16x32_bf16 v[6:9], v[178:181], v[250:253], v[6:9]
	v_mfma_f32_16x16x32_bf16 v[2:5], v[218:221], v[250:253], v[2:5]
	s_barrier
	s_setprio 0
	s_add_i32 vcc_hi, vcc_hi, 2
	s_add_u32 s62, s62, 0x10000
	s_addc_u32 s63, s63, 0
	s_add_u32 s61, s61, 0x10000
	s_addc_u32 vcc_lo, vcc_lo, 0
	s_cmp_gt_u32 vcc_hi, 29
	s_cbranch_scc0 .LBB0_171
	s_and_b64 vcc, exec, s[48:49]
	s_cbranch_vccz .LBB0_174
	s_barrier

.Lrx_hgrn1_w0:
	s_waitcnt vmcnt(24)
	s_waitcnt lgkmcnt(0)
	s_setprio 1
	s_barrier
	v_mfma_f32_16x16x32_bf16 v[128:131], v[132:135], v[202:205], v[128:131]
	v_mfma_f32_16x16x32_bf16 v[124:127], v[152:155], v[202:205], v[124:127]
	v_mfma_f32_16x16x32_bf16 v[110:113], v[132:135], v[210:213], v[110:113]
	v_mfma_f32_16x16x32_bf16 v[106:109], v[152:155], v[210:213], v[106:109]
	v_mfma_f32_16x16x32_bf16 v[94:97], v[132:135], v[218:221], v[94:97]
	v_mfma_f32_16x16x32_bf16 v[90:93], v[152:155], v[218:221], v[90:93]
	v_mfma_f32_16x16x32_bf16 v[78:81], v[132:135], v[226:229], v[78:81]
	v_mfma_f32_16x16x32_bf16 v[74:77], v[152:155], v[226:229], v[74:77]
	v_mfma_f32_16x16x32_bf16 v[128:131], v[136:139], v[206:209], v[128:131]
	v_mfma_f32_16x16x32_bf16 v[124:127], v[166:169], v[206:209], v[124:127]
	v_mfma_f32_16x16x32_bf16 v[110:113], v[136:139], v[214:217], v[110:113]
	v_mfma_f32_16x16x32_bf16 v[106:109], v[166:169], v[214:217], v[106:109]
	v_mfma_f32_16x16x32_bf16 v[94:97], v[136:139], v[222:225], v[94:97]
	v_mfma_f32_16x16x32_bf16 v[90:93], v[166:169], v[222:225], v[90:93]
	v_mfma_f32_16x16x32_bf16 v[78:81], v[136:139], v[230:233], v[78:81]
	v_mfma_f32_16x16x32_bf16 v[74:77], v[166:169], v[230:233], v[74:77]
	s_setprio 0
	s_setprio 1
	v_mfma_f32_16x16x32_bf16 v[120:123], v[176:179], v[202:205], v[120:123]
	v_mfma_f32_16x16x32_bf16 v[116:119], v[194:197], v[202:205], v[116:119]
	v_mfma_f32_16x16x32_bf16 v[102:105], v[176:179], v[210:213], v[102:105]
	v_mfma_f32_16x16x32_bf16 v[98:101], v[194:197], v[210:213], v[98:101]
	v_mfma_f32_16x16x32_bf16 v[86:89], v[176:179], v[218:221], v[86:89]
	v_mfma_f32_16x16x32_bf16 v[82:85], v[194:197], v[218:221], v[82:85]
	v_mfma_f32_16x16x32_bf16 v[70:73], v[176:179], v[226:229], v[70:73]
	v_mfma_f32_16x16x32_bf16 v[66:69], v[194:197], v[226:229], v[66:69]
	v_mfma_f32_16x16x32_bf16 v[120:123], v[180:183], v[206:209], v[120:123]
	v_mfma_f32_16x16x32_bf16 v[116:119], v[198:201], v[206:209], v[116:119]
	v_mfma_f32_16x16x32_bf16 v[102:105], v[180:183], v[214:217], v[102:105]
	v_mfma_f32_16x16x32_bf16 v[98:101], v[198:201], v[214:217], v[98:101]
	v_mfma_f32_16x16x32_bf16 v[86:89], v[180:183], v[222:225], v[86:89]
	v_mfma_f32_16x16x32_bf16 v[82:85], v[198:201], v[222:225], v[82:85]
	v_mfma_f32_16x16x32_bf16 v[70:73], v[180:183], v[230:233], v[70:73]
	v_mfma_f32_16x16x32_bf16 v[66:69], v[198:201], v[230:233], v[66:69]
	s_barrier
	s_setprio 0
	s_add_i32 s16, s16, s4
	v_lshl_add_u64 v[158:159], s[60:61], 0, v[142:143]
	s_mov_b32 m0, s16
	ds_read_b128 v[202:205], v175 offset:16384
	ds_read_b128 v[206:209], v175 offset:17408
	ds_read_b128 v[210:213], v175 offset:18432
	ds_read_b128 v[214:217], v175 offset:19456
	ds_read_b128 v[218:221], v175 offset:20480
	ds_read_b128 v[222:225], v175 offset:21504
	ds_read_b128 v[226:229], v175 offset:22528
	ds_read_b128 v[230:233], v175 offset:23552
	global_load_lds_dwordx4 v[158:159], off
	s_add_i32 m0, s16, 0x2000
	s_add_u32 s74, s60, 0x1000
	v_lshl_add_u64 v[158:159], s[60:61], 0, v[146:147]
	s_addc_u32 s75, s61, 0
	s_add_i32 s16, s17, s4
	global_load_lds_dwordx4 v[158:159], off
	v_lshl_add_u64 v[158:159], s[74:75], 0, v[142:143]
	s_mov_b32 m0, s16
	s_nop 0
	global_load_lds_dwordx4 v[158:159], off
	v_lshl_add_u64 v[158:159], s[74:75], 0, v[146:147]
	s_add_i32 m0, s16, 0x2000
	s_nop 0
	global_load_lds_dwordx4 v[158:159], off
	v_lshl_add_u64 v[158:159], s[62:63], 0, v[140:141]
	s_mov_b32 m0, s13
	s_nop 0
	global_load_lds_dwordx4 v[158:159], off
	v_lshl_add_u64 v[158:159], s[62:63], 0, v[144:145]
	s_mov_b32 m0, s20
	s_nop 0
	global_load_lds_dwordx4 v[158:159], off
	s_cmp_lg_u32 s32, 0
	s_cbranch_scc1 .Lrx_hgrn1_w1
	s_waitcnt vmcnt(8)
.Lrx_hgrn1_w1:
	s_waitcnt vmcnt(24)
	s_waitcnt lgkmcnt(0)
	s_setprio 1
	s_barrier
	v_mfma_f32_16x16x32_bf16 v[62:65], v[132:135], v[202:205], v[62:65]
	v_mfma_f32_16x16x32_bf16 v[58:61], v[152:155], v[202:205], v[58:61]
	v_mfma_f32_16x16x32_bf16 v[46:49], v[132:135], v[210:213], v[46:49]
	v_mfma_f32_16x16x32_bf16 v[42:45], v[152:155], v[210:213], v[42:45]
	v_mfma_f32_16x16x32_bf16 v[30:33], v[132:135], v[218:221], v[30:33]
	v_mfma_f32_16x16x32_bf16 v[26:29], v[152:155], v[218:221], v[26:29]
	v_mfma_f32_16x16x32_bf16 v[14:17], v[132:135], v[226:229], v[14:17]
	v_mfma_f32_16x16x32_bf16 v[10:13], v[152:155], v[226:229], v[10:13]
	v_mfma_f32_16x16x32_bf16 v[62:65], v[136:139], v[206:209], v[62:65]
	v_mfma_f32_16x16x32_bf16 v[58:61], v[166:169], v[206:209], v[58:61]
	v_mfma_f32_16x16x32_bf16 v[46:49], v[136:139], v[214:217], v[46:49]
	v_mfma_f32_16x16x32_bf16 v[42:45], v[166:169], v[214:217], v[42:45]
	v_mfma_f32_16x16x32_bf16 v[30:33], v[136:139], v[222:225], v[30:33]
	v_mfma_f32_16x16x32_bf16 v[26:29], v[166:169], v[222:225], v[26:29]
	v_mfma_f32_16x16x32_bf16 v[14:17], v[136:139], v[230:233], v[14:17]
	v_mfma_f32_16x16x32_bf16 v[10:13], v[166:169], v[230:233], v[10:13]
	s_setprio 0
	s_setprio 1
	v_mfma_f32_16x16x32_bf16 v[54:57], v[176:179], v[202:205], v[54:57]
	v_mfma_f32_16x16x32_bf16 v[50:53], v[194:197], v[202:205], v[50:53]
	v_mfma_f32_16x16x32_bf16 v[38:41], v[176:179], v[210:213], v[38:41]
	v_mfma_f32_16x16x32_bf16 v[34:37], v[194:197], v[210:213], v[34:37]
	v_mfma_f32_16x16x32_bf16 v[22:25], v[176:179], v[218:221], v[22:25]
	v_mfma_f32_16x16x32_bf16 v[18:21], v[194:197], v[218:221], v[18:21]
	v_mfma_f32_16x16x32_bf16 v[6:9], v[176:179], v[226:229], v[6:9]
	v_mfma_f32_16x16x32_bf16 v[2:5], v[194:197], v[226:229], v[2:5]
	v_mfma_f32_16x16x32_bf16 v[54:57], v[180:183], v[206:209], v[54:57]
	v_mfma_f32_16x16x32_bf16 v[50:53], v[198:201], v[206:209], v[50:53]
	v_mfma_f32_16x16x32_bf16 v[38:41], v[180:183], v[214:217], v[38:41]
	v_mfma_f32_16x16x32_bf16 v[34:37], v[198:201], v[214:217], v[34:37]
	v_mfma_f32_16x16x32_bf16 v[22:25], v[180:183], v[222:225], v[22:25]
	v_mfma_f32_16x16x32_bf16 v[18:21], v[198:201], v[222:225], v[18:21]
	v_mfma_f32_16x16x32_bf16 v[6:9], v[180:183], v[230:233], v[6:9]
	v_mfma_f32_16x16x32_bf16 v[2:5], v[198:201], v[230:233], v[2:5]
	s_barrier
	s_setprio 0
	s_add_i32 s16, 0, 0x18000
	v_add_u32_e32 v114, s16, v172
	s_add_i32 s17, 0, 0x1c000
	ds_read_b128 v[132:135], v114
	ds_read_b128 v[136:139], v114 offset:1024
	ds_read_b128 v[152:155], v114 offset:2048
	ds_read_b128 v[166:169], v114 offset:3072
	v_add_u32_e32 v114, s17, v172
	ds_read_b128 v[176:179], v114
	ds_read_b128 v[180:183], v114 offset:1024
	ds_read_b128 v[194:197], v114 offset:2048
	ds_read_b128 v[198:201], v114 offset:3072
	s_add_u32 s62, s62, 0x4000
	s_addc_u32 s63, s63, 0
	s_mov_b32 m0, s21
	v_lshl_add_u64 v[158:159], s[62:63], 0, v[140:141]
	ds_read_b128 v[202:205], v175 offset:32768
	ds_read_b128 v[206:209], v175 offset:33792
	ds_read_b128 v[210:213], v175 offset:34816
	ds_read_b128 v[214:217], v175 offset:35840
	ds_read_b128 v[218:221], v175 offset:36864
	ds_read_b128 v[222:225], v175 offset:37888
	ds_read_b128 v[226:229], v175 offset:38912
	ds_read_b128 v[230:233], v175 offset:39936
	global_load_lds_dwordx4 v[158:159], off
	v_lshl_add_u64 v[158:159], s[62:63], 0, v[144:145]
	s_mov_b32 m0, s24
	s_nop 0
	global_load_lds_dwordx4 v[158:159], off
	s_cmp_lg_u32 s32, 0
	s_cbranch_scc1 .Lrx_hgrn1_w2
	s_waitcnt vmcnt(8)
.Lrx_hgrn1_w2:
	s_waitcnt vmcnt(24)
	s_mov_b32 s32, 0
	s_waitcnt lgkmcnt(0)
	s_setprio 1
	s_barrier
	v_mfma_f32_16x16x32_bf16 v[128:131], v[132:135], v[202:205], v[128:131]
	v_mfma_f32_16x16x32_bf16 v[124:127], v[152:155], v[202:205], v[124:127]
	v_mfma_f32_16x16x32_bf16 v[110:113], v[132:135], v[210:213], v[110:113]
	v_mfma_f32_16x16x32_bf16 v[106:109], v[152:155], v[210:213], v[106:109]
	v_mfma_f32_16x16x32_bf16 v[94:97], v[132:135], v[218:221], v[94:97]
	v_mfma_f32_16x16x32_bf16 v[90:93], v[152:155], v[218:221], v[90:93]
	v_mfma_f32_16x16x32_bf16 v[78:81], v[132:135], v[226:229], v[78:81]
	v_mfma_f32_16x16x32_bf16 v[74:77], v[152:155], v[226:229], v[74:77]
	v_mfma_f32_16x16x32_bf16 v[128:131], v[136:139], v[206:209], v[128:131]
	v_mfma_f32_16x16x32_bf16 v[124:127], v[166:169], v[206:209], v[124:127]
	v_mfma_f32_16x16x32_bf16 v[110:113], v[136:139], v[214:217], v[110:113]
	v_mfma_f32_16x16x32_bf16 v[106:109], v[166:169], v[214:217], v[106:109]
	v_mfma_f32_16x16x32_bf16 v[94:97], v[136:139], v[222:225], v[94:97]
	v_mfma_f32_16x16x32_bf16 v[90:93], v[166:169], v[222:225], v[90:93]
	v_mfma_f32_16x16x32_bf16 v[78:81], v[136:139], v[230:233], v[78:81]
	v_mfma_f32_16x16x32_bf16 v[74:77], v[166:169], v[230:233], v[74:77]
	s_setprio 0
	s_setprio 1
	v_mfma_f32_16x16x32_bf16 v[120:123], v[176:179], v[202:205], v[120:123]
	v_mfma_f32_16x16x32_bf16 v[116:119], v[194:197], v[202:205], v[116:119]
	v_mfma_f32_16x16x32_bf16 v[102:105], v[176:179], v[210:213], v[102:105]
	v_mfma_f32_16x16x32_bf16 v[98:101], v[194:197], v[210:213], v[98:101]
	v_mfma_f32_16x16x32_bf16 v[86:89], v[176:179], v[218:221], v[86:89]
	v_mfma_f32_16x16x32_bf16 v[82:85], v[194:197], v[218:221], v[82:85]
	v_mfma_f32_16x16x32_bf16 v[70:73], v[176:179], v[226:229], v[70:73]
	v_mfma_f32_16x16x32_bf16 v[66:69], v[194:197], v[226:229], v[66:69]
	v_mfma_f32_16x16x32_bf16 v[120:123], v[180:183], v[206:209], v[120:123]
	v_mfma_f32_16x16x32_bf16 v[116:119], v[198:201], v[206:209], v[116:119]
	v_mfma_f32_16x16x32_bf16 v[102:105], v[180:183], v[214:217], v[102:105]
	v_mfma_f32_16x16x32_bf16 v[98:101], v[198:201], v[214:217], v[98:101]
	v_mfma_f32_16x16x32_bf16 v[86:89], v[180:183], v[222:225], v[86:89]
	v_mfma_f32_16x16x32_bf16 v[82:85], v[198:201], v[222:225], v[82:85]
	v_mfma_f32_16x16x32_bf16 v[70:73], v[180:183], v[230:233], v[70:73]
	v_mfma_f32_16x16x32_bf16 v[66:69], v[198:201], v[230:233], v[66:69]
	s_barrier
	s_setprio 0
	s_add_u32 s62, s60, 0x8000
	s_addc_u32 s63, s61, 0
	s_add_i32 s16, s16, s4
	v_lshl_add_u64 v[158:159], s[62:63], 0, v[142:143]
	s_mov_b32 m0, s16
	ds_read_b128 v[202:205], v175 offset:49152
	ds_read_b128 v[206:209], v175 offset:50176
	ds_read_b128 v[210:213], v175 offset:51200
	ds_read_b128 v[214:217], v175 offset:52224
	ds_read_b128 v[218:221], v175 offset:53248
	ds_read_b128 v[222:225], v175 offset:54272
	ds_read_b128 v[226:229], v175 offset:55296
	ds_read_b128 v[230:233], v175 offset:56320
	global_load_lds_dwordx4 v[158:159], off
	s_add_i32 m0, s16, 0x2000
	s_add_u32 s60, s60, 0x9000
	v_lshl_add_u64 v[158:159], s[62:63], 0, v[146:147]
	s_addc_u32 s61, s61, 0
	s_add_i32 s16, s17, s4
	global_load_lds_dwordx4 v[158:159], off
	v_lshl_add_u64 v[158:159], s[60:61], 0, v[142:143]
	s_mov_b32 m0, s16
	s_nop 0
	global_load_lds_dwordx4 v[158:159], off
	v_lshl_add_u64 v[158:159], s[60:61], 0, v[146:147]
	s_add_i32 m0, s16, 0x2000
	s_nop 0
	global_load_lds_dwordx4 v[158:159], off
	v_lshl_add_u64 v[158:159], s[58:59], 0, v[140:141]
	s_mov_b32 m0, s65
	s_nop 0
	global_load_lds_dwordx4 v[158:159], off
	v_lshl_add_u64 v[158:159], s[58:59], 0, v[144:145]
	s_mov_b32 m0, s66
	s_nop 0
	global_load_lds_dwordx4 v[158:159], off
	s_waitcnt vmcnt(8)
	s_waitcnt lgkmcnt(0)
	s_setprio 1
	s_barrier
	v_mfma_f32_16x16x32_bf16 v[62:65], v[132:135], v[202:205], v[62:65]
	v_mfma_f32_16x16x32_bf16 v[58:61], v[152:155], v[202:205], v[58:61]
	v_mfma_f32_16x16x32_bf16 v[46:49], v[132:135], v[210:213], v[46:49]
	v_mfma_f32_16x16x32_bf16 v[42:45], v[152:155], v[210:213], v[42:45]
	v_mfma_f32_16x16x32_bf16 v[30:33], v[132:135], v[218:221], v[30:33]
	v_mfma_f32_16x16x32_bf16 v[26:29], v[152:155], v[218:221], v[26:29]
	v_mfma_f32_16x16x32_bf16 v[14:17], v[132:135], v[226:229], v[14:17]
	v_mfma_f32_16x16x32_bf16 v[10:13], v[152:155], v[226:229], v[10:13]
	v_mfma_f32_16x16x32_bf16 v[62:65], v[136:139], v[206:209], v[62:65]
	v_mfma_f32_16x16x32_bf16 v[58:61], v[166:169], v[206:209], v[58:61]
	v_mfma_f32_16x16x32_bf16 v[46:49], v[136:139], v[214:217], v[46:49]
	v_mfma_f32_16x16x32_bf16 v[42:45], v[166:169], v[214:217], v[42:45]
	v_mfma_f32_16x16x32_bf16 v[30:33], v[136:139], v[222:225], v[30:33]
	v_mfma_f32_16x16x32_bf16 v[26:29], v[166:169], v[222:225], v[26:29]
	v_mfma_f32_16x16x32_bf16 v[14:17], v[136:139], v[230:233], v[14:17]
	v_mfma_f32_16x16x32_bf16 v[10:13], v[166:169], v[230:233], v[10:13]
	s_setprio 0
	s_setprio 1
	v_mfma_f32_16x16x32_bf16 v[54:57], v[176:179], v[202:205], v[54:57]
	v_mfma_f32_16x16x32_bf16 v[50:53], v[194:197], v[202:205], v[50:53]
	v_mfma_f32_16x16x32_bf16 v[38:41], v[176:179], v[210:213], v[38:41]
	v_mfma_f32_16x16x32_bf16 v[34:37], v[194:197], v[210:213], v[34:37]
	v_mfma_f32_16x16x32_bf16 v[22:25], v[176:179], v[218:221], v[22:25]
	v_mfma_f32_16x16x32_bf16 v[18:21], v[194:197], v[218:221], v[18:21]
	v_mfma_f32_16x16x32_bf16 v[6:9], v[176:179], v[226:229], v[6:9]
	v_mfma_f32_16x16x32_bf16 v[2:5], v[194:197], v[226:229], v[2:5]
	v_mfma_f32_16x16x32_bf16 v[54:57], v[180:183], v[206:209], v[54:57]
	v_mfma_f32_16x16x32_bf16 v[50:53], v[198:201], v[206:209], v[50:53]
	v_mfma_f32_16x16x32_bf16 v[38:41], v[180:183], v[214:217], v[38:41]
	v_mfma_f32_16x16x32_bf16 v[34:37], v[198:201], v[214:217], v[34:37]
	v_mfma_f32_16x16x32_bf16 v[22:25], v[180:183], v[222:225], v[22:25]
	v_mfma_f32_16x16x32_bf16 v[18:21], v[198:201], v[222:225], v[18:21]
	v_mfma_f32_16x16x32_bf16 v[6:9], v[180:183], v[230:233], v[6:9]
	v_mfma_f32_16x16x32_bf16 v[2:5], v[198:201], v[230:233], v[2:5]
	s_barrier
	s_setprio 0
	s_add_i32 s70, s70, 2
	s_add_u32 s56, s56, 0x10000
	s_addc_u32 s57, s57, 0
	s_add_u32 s51, s51, 0x10000
	s_addc_u32 s69, s69, 0
	s_cmp_gt_u32 s70, 29
	s_cbranch_scc0 .LBB0_346
	s_add_u32 s100, s29, 0xc000
	s_addc_u32 s101, s15, 0
	v_lshl_add_u64 v[158:159], s[100:101], 0, v[148:149]
	s_add_i32 m0, s13, 0xc000
	s_nop 0
	global_load_lds_dwordx4 v[158:159], off
	v_lshl_add_u64 v[158:159], s[100:101], 0, v[150:151]
	s_add_i32 m0, s13, 0xe000
	s_nop 0
	global_load_lds_dwordx4 v[158:159], off
	s_and_b64 vcc, exec, s[46:47]
	s_cbranch_vccz .LBB0_349
	s_barrier

.Lrx_hgrn2_w0:
	s_waitcnt vmcnt(24)
	s_waitcnt lgkmcnt(0)
	s_setprio 1
	s_barrier
	v_mfma_f32_16x16x32_bf16 v[128:131], v[132:135], v[202:205], v[128:131]
	v_mfma_f32_16x16x32_bf16 v[124:127], v[152:155], v[202:205], v[124:127]
	v_mfma_f32_16x16x32_bf16 v[110:113], v[132:135], v[210:213], v[110:113]
	v_mfma_f32_16x16x32_bf16 v[106:109], v[152:155], v[210:213], v[106:109]
	v_mfma_f32_16x16x32_bf16 v[94:97], v[132:135], v[218:221], v[94:97]
	v_mfma_f32_16x16x32_bf16 v[90:93], v[152:155], v[218:221], v[90:93]
	v_mfma_f32_16x16x32_bf16 v[78:81], v[132:135], v[226:229], v[78:81]
	v_mfma_f32_16x16x32_bf16 v[74:77], v[152:155], v[226:229], v[74:77]
	v_mfma_f32_16x16x32_bf16 v[128:131], v[136:139], v[206:209], v[128:131]
	v_mfma_f32_16x16x32_bf16 v[124:127], v[166:169], v[206:209], v[124:127]
	v_mfma_f32_16x16x32_bf16 v[110:113], v[136:139], v[214:217], v[110:113]
	v_mfma_f32_16x16x32_bf16 v[106:109], v[166:169], v[214:217], v[106:109]
	v_mfma_f32_16x16x32_bf16 v[94:97], v[136:139], v[222:225], v[94:97]
	v_mfma_f32_16x16x32_bf16 v[90:93], v[166:169], v[222:225], v[90:93]
	v_mfma_f32_16x16x32_bf16 v[78:81], v[136:139], v[230:233], v[78:81]
	v_mfma_f32_16x16x32_bf16 v[74:77], v[166:169], v[230:233], v[74:77]
	s_setprio 0
	s_setprio 1
	v_mfma_f32_16x16x32_bf16 v[120:123], v[176:179], v[202:205], v[120:123]
	v_mfma_f32_16x16x32_bf16 v[116:119], v[194:197], v[202:205], v[116:119]
	v_mfma_f32_16x16x32_bf16 v[102:105], v[176:179], v[210:213], v[102:105]
	v_mfma_f32_16x16x32_bf16 v[98:101], v[194:197], v[210:213], v[98:101]
	v_mfma_f32_16x16x32_bf16 v[86:89], v[176:179], v[218:221], v[86:89]
	v_mfma_f32_16x16x32_bf16 v[82:85], v[194:197], v[218:221], v[82:85]
	v_mfma_f32_16x16x32_bf16 v[70:73], v[176:179], v[226:229], v[70:73]
	v_mfma_f32_16x16x32_bf16 v[66:69], v[194:197], v[226:229], v[66:69]
	v_mfma_f32_16x16x32_bf16 v[120:123], v[180:183], v[206:209], v[120:123]
	v_mfma_f32_16x16x32_bf16 v[116:119], v[198:201], v[206:209], v[116:119]
	v_mfma_f32_16x16x32_bf16 v[102:105], v[180:183], v[214:217], v[102:105]
	v_mfma_f32_16x16x32_bf16 v[98:101], v[198:201], v[214:217], v[98:101]
	v_mfma_f32_16x16x32_bf16 v[86:89], v[180:183], v[222:225], v[86:89]
	v_mfma_f32_16x16x32_bf16 v[82:85], v[198:201], v[222:225], v[82:85]
	v_mfma_f32_16x16x32_bf16 v[70:73], v[180:183], v[230:233], v[70:73]
	v_mfma_f32_16x16x32_bf16 v[66:69], v[198:201], v[230:233], v[66:69]
	s_barrier
	s_setprio 0
	s_add_i32 s16, s16, s4
	v_lshl_add_u64 v[158:159], s[58:59], 0, v[142:143]
	s_mov_b32 m0, s16
	ds_read_b128 v[202:205], v175 offset:16384
	ds_read_b128 v[206:209], v175 offset:17408
	ds_read_b128 v[210:213], v175 offset:18432
	ds_read_b128 v[214:217], v175 offset:19456
	ds_read_b128 v[218:221], v175 offset:20480
	ds_read_b128 v[222:225], v175 offset:21504
	ds_read_b128 v[226:229], v175 offset:22528
	ds_read_b128 v[230:233], v175 offset:23552
	global_load_lds_dwordx4 v[158:159], off
	s_add_i32 m0, s16, 0x2000
	s_add_u32 s68, s58, 0x1000
	v_lshl_add_u64 v[158:159], s[58:59], 0, v[146:147]
	s_addc_u32 s69, s59, 0
	s_add_i32 s16, s17, s4
	global_load_lds_dwordx4 v[158:159], off
	v_lshl_add_u64 v[158:159], s[68:69], 0, v[142:143]
	s_mov_b32 m0, s16
	s_nop 0
	global_load_lds_dwordx4 v[158:159], off
	v_lshl_add_u64 v[158:159], s[68:69], 0, v[146:147]
	s_add_i32 m0, s16, 0x2000
	s_nop 0
	global_load_lds_dwordx4 v[158:159], off
	v_lshl_add_u64 v[158:159], s[60:61], 0, v[140:141]
	s_mov_b32 m0, s12
	s_nop 0
	global_load_lds_dwordx4 v[158:159], off
	v_lshl_add_u64 v[158:159], s[60:61], 0, v[144:145]
	s_mov_b32 m0, s13
	s_nop 0
	global_load_lds_dwordx4 v[158:159], off
	s_cmp_lg_u32 s32, 0
	s_cbranch_scc1 .Lrx_hgrn2_w1
	s_waitcnt vmcnt(8)
.Lrx_hgrn2_w1:
	s_waitcnt vmcnt(24)
	s_waitcnt lgkmcnt(0)
	s_setprio 1
	s_barrier
	v_mfma_f32_16x16x32_bf16 v[62:65], v[132:135], v[202:205], v[62:65]
	v_mfma_f32_16x16x32_bf16 v[58:61], v[152:155], v[202:205], v[58:61]
	v_mfma_f32_16x16x32_bf16 v[46:49], v[132:135], v[210:213], v[46:49]
	v_mfma_f32_16x16x32_bf16 v[42:45], v[152:155], v[210:213], v[42:45]
	v_mfma_f32_16x16x32_bf16 v[30:33], v[132:135], v[218:221], v[30:33]
	v_mfma_f32_16x16x32_bf16 v[26:29], v[152:155], v[218:221], v[26:29]
	v_mfma_f32_16x16x32_bf16 v[14:17], v[132:135], v[226:229], v[14:17]
	v_mfma_f32_16x16x32_bf16 v[10:13], v[152:155], v[226:229], v[10:13]
	v_mfma_f32_16x16x32_bf16 v[62:65], v[136:139], v[206:209], v[62:65]
	v_mfma_f32_16x16x32_bf16 v[58:61], v[166:169], v[206:209], v[58:61]
	v_mfma_f32_16x16x32_bf16 v[46:49], v[136:139], v[214:217], v[46:49]
	v_mfma_f32_16x16x32_bf16 v[42:45], v[166:169], v[214:217], v[42:45]
	v_mfma_f32_16x16x32_bf16 v[30:33], v[136:139], v[222:225], v[30:33]
	v_mfma_f32_16x16x32_bf16 v[26:29], v[166:169], v[222:225], v[26:29]
	v_mfma_f32_16x16x32_bf16 v[14:17], v[136:139], v[230:233], v[14:17]
	v_mfma_f32_16x16x32_bf16 v[10:13], v[166:169], v[230:233], v[10:13]
	s_setprio 0
	s_setprio 1
	v_mfma_f32_16x16x32_bf16 v[54:57], v[176:179], v[202:205], v[54:57]
	v_mfma_f32_16x16x32_bf16 v[50:53], v[194:197], v[202:205], v[50:53]
	v_mfma_f32_16x16x32_bf16 v[38:41], v[176:179], v[210:213], v[38:41]
	v_mfma_f32_16x16x32_bf16 v[34:37], v[194:197], v[210:213], v[34:37]
	v_mfma_f32_16x16x32_bf16 v[22:25], v[176:179], v[218:221], v[22:25]
	v_mfma_f32_16x16x32_bf16 v[18:21], v[194:197], v[218:221], v[18:21]
	v_mfma_f32_16x16x32_bf16 v[6:9], v[176:179], v[226:229], v[6:9]
	v_mfma_f32_16x16x32_bf16 v[2:5], v[194:197], v[226:229], v[2:5]
	v_mfma_f32_16x16x32_bf16 v[54:57], v[180:183], v[206:209], v[54:57]
	v_mfma_f32_16x16x32_bf16 v[50:53], v[198:201], v[206:209], v[50:53]
	v_mfma_f32_16x16x32_bf16 v[38:41], v[180:183], v[214:217], v[38:41]
	v_mfma_f32_16x16x32_bf16 v[34:37], v[198:201], v[214:217], v[34:37]
	v_mfma_f32_16x16x32_bf16 v[22:25], v[180:183], v[222:225], v[22:25]
	v_mfma_f32_16x16x32_bf16 v[18:21], v[198:201], v[222:225], v[18:21]
	v_mfma_f32_16x16x32_bf16 v[6:9], v[180:183], v[230:233], v[6:9]
	v_mfma_f32_16x16x32_bf16 v[2:5], v[198:201], v[230:233], v[2:5]
	s_barrier
	s_setprio 0
	s_add_i32 s16, 0, 0x18000
	v_add_u32_e32 v114, s16, v172
	s_add_i32 s17, 0, 0x1c000
	ds_read_b128 v[132:135], v114
	ds_read_b128 v[136:139], v114 offset:1024
	ds_read_b128 v[152:155], v114 offset:2048
	ds_read_b128 v[166:169], v114 offset:3072
	v_add_u32_e32 v114, s17, v172
	ds_read_b128 v[176:179], v114
	ds_read_b128 v[180:183], v114 offset:1024
	ds_read_b128 v[194:197], v114 offset:2048
	ds_read_b128 v[198:201], v114 offset:3072
	s_add_u32 s60, s60, 0x4000
	s_addc_u32 s61, s61, 0
	s_mov_b32 m0, s20
	v_lshl_add_u64 v[158:159], s[60:61], 0, v[140:141]
	ds_read_b128 v[202:205], v175 offset:32768
	ds_read_b128 v[206:209], v175 offset:33792
	ds_read_b128 v[210:213], v175 offset:34816
	ds_read_b128 v[214:217], v175 offset:35840
	ds_read_b128 v[218:221], v175 offset:36864
	ds_read_b128 v[222:225], v175 offset:37888
	ds_read_b128 v[226:229], v175 offset:38912
	ds_read_b128 v[230:233], v175 offset:39936
	global_load_lds_dwordx4 v[158:159], off
	v_lshl_add_u64 v[158:159], s[60:61], 0, v[144:145]
	s_mov_b32 m0, s21
	s_nop 0
	global_load_lds_dwordx4 v[158:159], off
	s_cmp_lg_u32 s32, 0
	s_cbranch_scc1 .Lrx_hgrn2_w2
	s_waitcnt vmcnt(8)
.Lrx_hgrn2_w2:
	s_waitcnt vmcnt(24)
	s_mov_b32 s32, 0
	s_waitcnt lgkmcnt(0)
	s_setprio 1
	s_barrier
	v_mfma_f32_16x16x32_bf16 v[128:131], v[132:135], v[202:205], v[128:131]
	v_mfma_f32_16x16x32_bf16 v[124:127], v[152:155], v[202:205], v[124:127]
	v_mfma_f32_16x16x32_bf16 v[110:113], v[132:135], v[210:213], v[110:113]
	v_mfma_f32_16x16x32_bf16 v[106:109], v[152:155], v[210:213], v[106:109]
	v_mfma_f32_16x16x32_bf16 v[94:97], v[132:135], v[218:221], v[94:97]
	v_mfma_f32_16x16x32_bf16 v[90:93], v[152:155], v[218:221], v[90:93]
	v_mfma_f32_16x16x32_bf16 v[78:81], v[132:135], v[226:229], v[78:81]
	v_mfma_f32_16x16x32_bf16 v[74:77], v[152:155], v[226:229], v[74:77]
	v_mfma_f32_16x16x32_bf16 v[128:131], v[136:139], v[206:209], v[128:131]
	v_mfma_f32_16x16x32_bf16 v[124:127], v[166:169], v[206:209], v[124:127]
	v_mfma_f32_16x16x32_bf16 v[110:113], v[136:139], v[214:217], v[110:113]
	v_mfma_f32_16x16x32_bf16 v[106:109], v[166:169], v[214:217], v[106:109]
	v_mfma_f32_16x16x32_bf16 v[94:97], v[136:139], v[222:225], v[94:97]
	v_mfma_f32_16x16x32_bf16 v[90:93], v[166:169], v[222:225], v[90:93]
	v_mfma_f32_16x16x32_bf16 v[78:81], v[136:139], v[230:233], v[78:81]
	v_mfma_f32_16x16x32_bf16 v[74:77], v[166:169], v[230:233], v[74:77]
	s_setprio 0
	s_setprio 1
	v_mfma_f32_16x16x32_bf16 v[120:123], v[176:179], v[202:205], v[120:123]
	v_mfma_f32_16x16x32_bf16 v[116:119], v[194:197], v[202:205], v[116:119]
	v_mfma_f32_16x16x32_bf16 v[102:105], v[176:179], v[210:213], v[102:105]
	v_mfma_f32_16x16x32_bf16 v[98:101], v[194:197], v[210:213], v[98:101]
	v_mfma_f32_16x16x32_bf16 v[86:89], v[176:179], v[218:221], v[86:89]
	v_mfma_f32_16x16x32_bf16 v[82:85], v[194:197], v[218:221], v[82:85]
	v_mfma_f32_16x16x32_bf16 v[70:73], v[176:179], v[226:229], v[70:73]
	v_mfma_f32_16x16x32_bf16 v[66:69], v[194:197], v[226:229], v[66:69]
	v_mfma_f32_16x16x32_bf16 v[120:123], v[180:183], v[206:209], v[120:123]
	v_mfma_f32_16x16x32_bf16 v[116:119], v[198:201], v[206:209], v[116:119]
	v_mfma_f32_16x16x32_bf16 v[102:105], v[180:183], v[214:217], v[102:105]
	v_mfma_f32_16x16x32_bf16 v[98:101], v[198:201], v[214:217], v[98:101]
	v_mfma_f32_16x16x32_bf16 v[86:89], v[180:183], v[222:225], v[86:89]
	v_mfma_f32_16x16x32_bf16 v[82:85], v[198:201], v[222:225], v[82:85]
	v_mfma_f32_16x16x32_bf16 v[70:73], v[180:183], v[230:233], v[70:73]
	v_mfma_f32_16x16x32_bf16 v[66:69], v[198:201], v[230:233], v[66:69]
	s_barrier
	s_setprio 0
	s_add_u32 s60, s58, 0x8000
	s_addc_u32 s61, s59, 0
	s_add_i32 s16, s16, s4
	v_lshl_add_u64 v[158:159], s[60:61], 0, v[142:143]
	s_mov_b32 m0, s16
	ds_read_b128 v[202:205], v175 offset:49152
	ds_read_b128 v[206:209], v175 offset:50176
	ds_read_b128 v[210:213], v175 offset:51200
	ds_read_b128 v[214:217], v175 offset:52224
	ds_read_b128 v[218:221], v175 offset:53248
	ds_read_b128 v[222:225], v175 offset:54272
	ds_read_b128 v[226:229], v175 offset:55296
	ds_read_b128 v[230:233], v175 offset:56320
	global_load_lds_dwordx4 v[158:159], off
	s_add_i32 m0, s16, 0x2000
	s_add_u32 s58, s58, 0x9000
	v_lshl_add_u64 v[158:159], s[60:61], 0, v[146:147]
	s_addc_u32 s59, s59, 0
	s_add_i32 s16, s17, s4
	global_load_lds_dwordx4 v[158:159], off
	v_lshl_add_u64 v[158:159], s[58:59], 0, v[142:143]
	s_mov_b32 m0, s16
	s_nop 0
	global_load_lds_dwordx4 v[158:159], off
	v_lshl_add_u64 v[158:159], s[58:59], 0, v[146:147]
	s_add_i32 m0, s16, 0x2000
	s_nop 0
	global_load_lds_dwordx4 v[158:159], off
	v_lshl_add_u64 v[158:159], s[56:57], 0, v[140:141]
	s_mov_b32 m0, s62
	s_nop 0
	global_load_lds_dwordx4 v[158:159], off
	v_lshl_add_u64 v[158:159], s[56:57], 0, v[144:145]
	s_mov_b32 m0, s63
	s_nop 0
	global_load_lds_dwordx4 v[158:159], off
	s_waitcnt vmcnt(8)
	s_waitcnt lgkmcnt(0)
	s_setprio 1
	s_barrier
	v_mfma_f32_16x16x32_bf16 v[62:65], v[132:135], v[202:205], v[62:65]
	v_mfma_f32_16x16x32_bf16 v[58:61], v[152:155], v[202:205], v[58:61]
	v_mfma_f32_16x16x32_bf16 v[46:49], v[132:135], v[210:213], v[46:49]
	v_mfma_f32_16x16x32_bf16 v[42:45], v[152:155], v[210:213], v[42:45]
	v_mfma_f32_16x16x32_bf16 v[30:33], v[132:135], v[218:221], v[30:33]
	v_mfma_f32_16x16x32_bf16 v[26:29], v[152:155], v[218:221], v[26:29]
	v_mfma_f32_16x16x32_bf16 v[14:17], v[132:135], v[226:229], v[14:17]
	v_mfma_f32_16x16x32_bf16 v[10:13], v[152:155], v[226:229], v[10:13]
	v_mfma_f32_16x16x32_bf16 v[62:65], v[136:139], v[206:209], v[62:65]
	v_mfma_f32_16x16x32_bf16 v[58:61], v[166:169], v[206:209], v[58:61]
	v_mfma_f32_16x16x32_bf16 v[46:49], v[136:139], v[214:217], v[46:49]
	v_mfma_f32_16x16x32_bf16 v[42:45], v[166:169], v[214:217], v[42:45]
	v_mfma_f32_16x16x32_bf16 v[30:33], v[136:139], v[222:225], v[30:33]
	v_mfma_f32_16x16x32_bf16 v[26:29], v[166:169], v[222:225], v[26:29]
	v_mfma_f32_16x16x32_bf16 v[14:17], v[136:139], v[230:233], v[14:17]
	v_mfma_f32_16x16x32_bf16 v[10:13], v[166:169], v[230:233], v[10:13]
	s_setprio 0
	s_setprio 1
	v_mfma_f32_16x16x32_bf16 v[54:57], v[176:179], v[202:205], v[54:57]
	v_mfma_f32_16x16x32_bf16 v[50:53], v[194:197], v[202:205], v[50:53]
	v_mfma_f32_16x16x32_bf16 v[38:41], v[176:179], v[210:213], v[38:41]
	v_mfma_f32_16x16x32_bf16 v[34:37], v[194:197], v[210:213], v[34:37]
	v_mfma_f32_16x16x32_bf16 v[22:25], v[176:179], v[218:221], v[22:25]
	v_mfma_f32_16x16x32_bf16 v[18:21], v[194:197], v[218:221], v[18:21]
	v_mfma_f32_16x16x32_bf16 v[6:9], v[176:179], v[226:229], v[6:9]
	v_mfma_f32_16x16x32_bf16 v[2:5], v[194:197], v[226:229], v[2:5]
	v_mfma_f32_16x16x32_bf16 v[54:57], v[180:183], v[206:209], v[54:57]
	v_mfma_f32_16x16x32_bf16 v[50:53], v[198:201], v[206:209], v[50:53]
	v_mfma_f32_16x16x32_bf16 v[38:41], v[180:183], v[214:217], v[38:41]
	v_mfma_f32_16x16x32_bf16 v[34:37], v[198:201], v[214:217], v[34:37]
	v_mfma_f32_16x16x32_bf16 v[22:25], v[180:183], v[222:225], v[22:25]
	v_mfma_f32_16x16x32_bf16 v[18:21], v[198:201], v[222:225], v[18:21]
	v_mfma_f32_16x16x32_bf16 v[6:9], v[180:183], v[230:233], v[6:9]
	v_mfma_f32_16x16x32_bf16 v[2:5], v[198:201], v[230:233], v[2:5]
	s_barrier
	s_setprio 0
	s_add_i32 s67, s67, 2
	s_add_u32 s54, s54, 0x10000
	s_addc_u32 s55, s55, 0
	s_add_u32 s49, s49, 0x10000
	s_addc_u32 s66, s66, 0
	s_cmp_gt_u32 s67, 29
	s_cbranch_scc0 .LBB0_503
	s_add_u32 s100, s29, 0xc000
	s_addc_u32 s101, s15, 0
	v_lshl_add_u64 v[158:159], s[100:101], 0, v[148:149]
	s_add_i32 m0, s12, 0xc000
	s_nop 0
	global_load_lds_dwordx4 v[158:159], off
	v_lshl_add_u64 v[158:159], s[100:101], 0, v[150:151]
	s_add_i32 m0, s12, 0xe000
	s_nop 0
	global_load_lds_dwordx4 v[158:159], off
	s_and_b64 vcc, exec, s[44:45]
	s_cbranch_vccz .LBB0_506
	s_barrier

.LBB0_1079:
	s_add_u32 s16, s52, 0x4000
	s_addc_u32 s17, s53, 0
	s_cmp_eq_u32 s64, 28
	s_cselect_b32 s56, s29, s16
	s_cselect_b32 s57, s24, s17
	s_cselect_b32 s55, s27, s63
	s_cselect_b32 s54, s47, s49
	s_add_u32 s50, s56, 0x8000
	s_addc_u32 s51, s57, 0
	s_add_i32 s16, 0, 0x10000
	v_add_u32_e32 v144, s16, v146
	s_add_i32 s65, 0, 0x14000
	ds_read_b128 v[148:151], v144
	ds_read_b128 v[152:155], v144 offset:1024
	ds_read_b128 v[158:161], v144 offset:2048
	ds_read_b128 v[166:169], v144 offset:3072
	v_add_u32_e32 v144, s65, v146
	ds_read_b128 v[170:173], v144
	ds_read_b128 v[174:177], v144 offset:1024
	ds_read_b128 v[178:181], v144 offset:2048
	ds_read_b128 v[194:197], v144 offset:3072
	v_lshl_add_u64 v[144:145], s[52:53], 0, v[140:141]
	s_add_i32 m0, s20, 0xc000
	ds_read_b128 v[198:201], v147
	ds_read_b128 v[202:205], v147 offset:1024
	ds_read_b128 v[206:209], v147 offset:2048
	ds_read_b128 v[210:213], v147 offset:3072
	ds_read_b128 v[214:217], v147 offset:4096
	ds_read_b128 v[218:221], v147 offset:5120
	ds_read_b128 v[222:225], v147 offset:6144
	ds_read_b128 v[226:229], v147 offset:7168
	global_load_lds_dwordx4 v[144:145], off
	v_lshl_add_u64 v[144:145], s[52:53], 0, v[142:143]
	s_add_i32 m0, s20, 0xe000
	s_nop 0
	global_load_lds_dwordx4 v[144:145], off
	s_waitcnt vmcnt(8)
	s_waitcnt lgkmcnt(0)
	s_setprio 1
	s_barrier
	v_mfma_f32_16x16x32_bf16 v[116:119], v[148:151], v[198:201], v[116:119]
	v_mfma_f32_16x16x32_bf16 v[124:127], v[158:161], v[198:201], v[124:127]
	v_mfma_f32_16x16x32_bf16 v[98:101], v[148:151], v[206:209], v[98:101]
	v_mfma_f32_16x16x32_bf16 v[102:105], v[158:161], v[206:209], v[102:105]
	v_mfma_f32_16x16x32_bf16 v[82:85], v[148:151], v[214:217], v[82:85]
	v_mfma_f32_16x16x32_bf16 v[90:93], v[158:161], v[214:217], v[90:93]
	v_mfma_f32_16x16x32_bf16 v[58:61], v[148:151], v[222:225], v[58:61]
	v_mfma_f32_16x16x32_bf16 v[70:73], v[158:161], v[222:225], v[70:73]
	v_mfma_f32_16x16x32_bf16 v[116:119], v[152:155], v[202:205], v[116:119]
	v_mfma_f32_16x16x32_bf16 v[124:127], v[166:169], v[202:205], v[124:127]
	v_mfma_f32_16x16x32_bf16 v[98:101], v[152:155], v[210:213], v[98:101]
	v_mfma_f32_16x16x32_bf16 v[102:105], v[166:169], v[210:213], v[102:105]
	v_mfma_f32_16x16x32_bf16 v[82:85], v[152:155], v[218:221], v[82:85]
	v_mfma_f32_16x16x32_bf16 v[90:93], v[166:169], v[218:221], v[90:93]
	v_mfma_f32_16x16x32_bf16 v[58:61], v[152:155], v[226:229], v[58:61]
	v_mfma_f32_16x16x32_bf16 v[70:73], v[166:169], v[226:229], v[70:73]
	s_setprio 0
	s_setprio 1
	v_mfma_f32_16x16x32_bf16 v[120:123], v[170:173], v[198:201], v[120:123]
	v_mfma_f32_16x16x32_bf16 v[128:131], v[178:181], v[198:201], v[128:131]
	v_mfma_f32_16x16x32_bf16 v[106:109], v[170:173], v[206:209], v[106:109]
	v_mfma_f32_16x16x32_bf16 v[110:113], v[178:181], v[206:209], v[110:113]
	v_mfma_f32_16x16x32_bf16 v[86:89], v[170:173], v[214:217], v[86:89]
	v_mfma_f32_16x16x32_bf16 v[94:97], v[178:181], v[214:217], v[94:97]
	v_mfma_f32_16x16x32_bf16 v[74:77], v[170:173], v[222:225], v[74:77]
	v_mfma_f32_16x16x32_bf16 v[78:81], v[178:181], v[222:225], v[78:81]
	v_mfma_f32_16x16x32_bf16 v[120:123], v[174:177], v[202:205], v[120:123]
	v_mfma_f32_16x16x32_bf16 v[128:131], v[194:197], v[202:205], v[128:131]
	v_mfma_f32_16x16x32_bf16 v[106:109], v[174:177], v[210:213], v[106:109]
	v_mfma_f32_16x16x32_bf16 v[110:113], v[194:197], v[210:213], v[110:113]
	v_mfma_f32_16x16x32_bf16 v[86:89], v[174:177], v[218:221], v[86:89]
	v_mfma_f32_16x16x32_bf16 v[94:97], v[194:197], v[218:221], v[94:97]
	v_mfma_f32_16x16x32_bf16 v[74:77], v[174:177], v[226:229], v[74:77]
	v_mfma_f32_16x16x32_bf16 v[78:81], v[194:197], v[226:229], v[78:81]
	s_barrier
	s_setprio 0
	s_add_i32 s16, s16, s13
	v_lshl_add_u64 v[144:145], s[54:55], 0, v[114:115]
	s_mov_b32 m0, s16
	ds_read_b128 v[198:201], v147 offset:16384
	ds_read_b128 v[202:205], v147 offset:17408
	ds_read_b128 v[206:209], v147 offset:18432
	ds_read_b128 v[210:213], v147 offset:19456
	ds_read_b128 v[214:217], v147 offset:20480
	ds_read_b128 v[218:221], v147 offset:21504
	ds_read_b128 v[222:225], v147 offset:22528
	ds_read_b128 v[226:229], v147 offset:23552
	global_load_lds_dwordx4 v[144:145], off
	s_add_i32 m0, s16, 0x2000
	s_add_u32 s16, s54, 0x1000
	v_lshl_add_u64 v[144:145], s[54:55], 0, v[136:137]
	s_addc_u32 s17, s55, 0
	s_add_i32 s65, s65, s13
	global_load_lds_dwordx4 v[144:145], off
	v_lshl_add_u64 v[144:145], s[16:17], 0, v[114:115]
	s_mov_b32 m0, s65
	s_nop 0
	global_load_lds_dwordx4 v[144:145], off
	v_lshl_add_u64 v[144:145], s[16:17], 0, v[136:137]
	s_add_i32 m0, s65, 0x2000
	s_nop 0
	global_load_lds_dwordx4 v[144:145], off
	v_lshl_add_u64 v[144:145], s[56:57], 0, v[132:133]
	s_mov_b32 m0, s20
	s_nop 0
	global_load_lds_dwordx4 v[144:145], off
	v_lshl_add_u64 v[144:145], s[56:57], 0, v[134:135]
	s_mov_b32 m0, s21
	s_nop 0
	global_load_lds_dwordx4 v[144:145], off
	s_waitcnt vmcnt(8)
	s_waitcnt lgkmcnt(0)
	s_setprio 1
	s_barrier
	v_mfma_f32_16x16x32_bf16 v[50:53], v[148:151], v[198:201], v[50:53]
	v_mfma_f32_16x16x32_bf16 v[62:65], v[158:161], v[198:201], v[62:65]
	v_mfma_f32_16x16x32_bf16 v[34:37], v[148:151], v[206:209], v[34:37]
	v_mfma_f32_16x16x32_bf16 v[38:41], v[158:161], v[206:209], v[38:41]
	v_mfma_f32_16x16x32_bf16 v[18:21], v[148:151], v[214:217], v[18:21]
	v_mfma_f32_16x16x32_bf16 v[26:29], v[158:161], v[214:217], v[26:29]
	v_mfma_f32_16x16x32_bf16 v[2:5], v[148:151], v[222:225], v[2:5]
	v_mfma_f32_16x16x32_bf16 v[6:9], v[158:161], v[222:225], v[6:9]
	v_mfma_f32_16x16x32_bf16 v[50:53], v[152:155], v[202:205], v[50:53]
	v_mfma_f32_16x16x32_bf16 v[62:65], v[166:169], v[202:205], v[62:65]
	v_mfma_f32_16x16x32_bf16 v[34:37], v[152:155], v[210:213], v[34:37]
	v_mfma_f32_16x16x32_bf16 v[38:41], v[166:169], v[210:213], v[38:41]
	v_mfma_f32_16x16x32_bf16 v[18:21], v[152:155], v[218:221], v[18:21]
	v_mfma_f32_16x16x32_bf16 v[26:29], v[166:169], v[218:221], v[26:29]
	v_mfma_f32_16x16x32_bf16 v[2:5], v[152:155], v[226:229], v[2:5]
	v_mfma_f32_16x16x32_bf16 v[6:9], v[166:169], v[226:229], v[6:9]
	s_setprio 0
	s_setprio 1
	v_mfma_f32_16x16x32_bf16 v[54:57], v[170:173], v[198:201], v[54:57]
	v_mfma_f32_16x16x32_bf16 v[66:69], v[178:181], v[198:201], v[66:69]
	v_mfma_f32_16x16x32_bf16 v[42:45], v[170:173], v[206:209], v[42:45]
	v_mfma_f32_16x16x32_bf16 v[46:49], v[178:181], v[206:209], v[46:49]
	v_mfma_f32_16x16x32_bf16 v[22:25], v[170:173], v[214:217], v[22:25]
	v_mfma_f32_16x16x32_bf16 v[30:33], v[178:181], v[214:217], v[30:33]
	v_mfma_f32_16x16x32_bf16 v[10:13], v[170:173], v[222:225], v[10:13]
	v_mfma_f32_16x16x32_bf16 v[14:17], v[178:181], v[222:225], v[14:17]
	v_mfma_f32_16x16x32_bf16 v[54:57], v[174:177], v[202:205], v[54:57]
	v_mfma_f32_16x16x32_bf16 v[66:69], v[194:197], v[202:205], v[66:69]
	v_mfma_f32_16x16x32_bf16 v[42:45], v[174:177], v[210:213], v[42:45]
	v_mfma_f32_16x16x32_bf16 v[46:49], v[194:197], v[210:213], v[46:49]
	v_mfma_f32_16x16x32_bf16 v[22:25], v[174:177], v[218:221], v[22:25]
	v_mfma_f32_16x16x32_bf16 v[30:33], v[194:197], v[218:221], v[30:33]
	v_mfma_f32_16x16x32_bf16 v[10:13], v[174:177], v[226:229], v[10:13]
	v_mfma_f32_16x16x32_bf16 v[14:17], v[194:197], v[226:229], v[14:17]
	s_barrier
	s_setprio 0
	s_add_i32 s65, 0, 0x18000
	v_add_u32_e32 v144, s65, v146
	s_add_i32 s66, 0, 0x1c000
	ds_read_b128 v[148:151], v144
	ds_read_b128 v[152:155], v144 offset:1024
	ds_read_b128 v[158:161], v144 offset:2048
	ds_read_b128 v[166:169], v144 offset:3072
	v_add_u32_e32 v144, s66, v146
	ds_read_b128 v[170:173], v144
	ds_read_b128 v[174:177], v144 offset:1024
	ds_read_b128 v[178:181], v144 offset:2048
	ds_read_b128 v[194:197], v144 offset:3072
	s_add_u32 s16, s56, 0x4000
	s_addc_u32 s17, s57, 0
	s_mov_b32 m0, s37
	v_lshl_add_u64 v[144:145], s[16:17], 0, v[132:133]
	ds_read_b128 v[198:201], v147 offset:32768
	ds_read_b128 v[202:205], v147 offset:33792
	ds_read_b128 v[206:209], v147 offset:34816
	ds_read_b128 v[210:213], v147 offset:35840
	ds_read_b128 v[214:217], v147 offset:36864
	ds_read_b128 v[218:221], v147 offset:37888
	ds_read_b128 v[222:225], v147 offset:38912
	ds_read_b128 v[226:229], v147 offset:39936
	global_load_lds_dwordx4 v[144:145], off
	v_lshl_add_u64 v[144:145], s[16:17], 0, v[134:135]
	s_mov_b32 m0, s58
	s_nop 0
	global_load_lds_dwordx4 v[144:145], off
	s_waitcnt vmcnt(8)
	s_waitcnt lgkmcnt(0)
	s_setprio 1
	s_barrier
	v_mfma_f32_16x16x32_bf16 v[116:119], v[148:151], v[198:201], v[116:119]
	v_mfma_f32_16x16x32_bf16 v[124:127], v[158:161], v[198:201], v[124:127]
	v_mfma_f32_16x16x32_bf16 v[98:101], v[148:151], v[206:209], v[98:101]
	v_mfma_f32_16x16x32_bf16 v[102:105], v[158:161], v[206:209], v[102:105]
	v_mfma_f32_16x16x32_bf16 v[82:85], v[148:151], v[214:217], v[82:85]
	v_mfma_f32_16x16x32_bf16 v[90:93], v[158:161], v[214:217], v[90:93]
	v_mfma_f32_16x16x32_bf16 v[58:61], v[148:151], v[222:225], v[58:61]
	v_mfma_f32_16x16x32_bf16 v[70:73], v[158:161], v[222:225], v[70:73]
	v_mfma_f32_16x16x32_bf16 v[116:119], v[152:155], v[202:205], v[116:119]
	v_mfma_f32_16x16x32_bf16 v[124:127], v[166:169], v[202:205], v[124:127]
	v_mfma_f32_16x16x32_bf16 v[98:101], v[152:155], v[210:213], v[98:101]
	v_mfma_f32_16x16x32_bf16 v[102:105], v[166:169], v[210:213], v[102:105]
	v_mfma_f32_16x16x32_bf16 v[82:85], v[152:155], v[218:221], v[82:85]
	v_mfma_f32_16x16x32_bf16 v[90:93], v[166:169], v[218:221], v[90:93]
	v_mfma_f32_16x16x32_bf16 v[58:61], v[152:155], v[226:229], v[58:61]
	v_mfma_f32_16x16x32_bf16 v[70:73], v[166:169], v[226:229], v[70:73]
	s_setprio 0
	s_setprio 1
	v_mfma_f32_16x16x32_bf16 v[120:123], v[170:173], v[198:201], v[120:123]
	v_mfma_f32_16x16x32_bf16 v[128:131], v[178:181], v[198:201], v[128:131]
	v_mfma_f32_16x16x32_bf16 v[106:109], v[170:173], v[206:209], v[106:109]
	v_mfma_f32_16x16x32_bf16 v[110:113], v[178:181], v[206:209], v[110:113]
	v_mfma_f32_16x16x32_bf16 v[86:89], v[170:173], v[214:217], v[86:89]
	v_mfma_f32_16x16x32_bf16 v[94:97], v[178:181], v[214:217], v[94:97]
	v_mfma_f32_16x16x32_bf16 v[74:77], v[170:173], v[222:225], v[74:77]
	v_mfma_f32_16x16x32_bf16 v[78:81], v[178:181], v[222:225], v[78:81]
	v_mfma_f32_16x16x32_bf16 v[120:123], v[174:177], v[202:205], v[120:123]
	v_mfma_f32_16x16x32_bf16 v[128:131], v[194:197], v[202:205], v[128:131]
	v_mfma_f32_16x16x32_bf16 v[106:109], v[174:177], v[210:213], v[106:109]
	v_mfma_f32_16x16x32_bf16 v[110:113], v[194:197], v[210:213], v[110:113]
	v_mfma_f32_16x16x32_bf16 v[86:89], v[174:177], v[218:221], v[86:89]
	v_mfma_f32_16x16x32_bf16 v[94:97], v[194:197], v[218:221], v[94:97]
	v_mfma_f32_16x16x32_bf16 v[74:77], v[174:177], v[226:229], v[74:77]
	v_mfma_f32_16x16x32_bf16 v[78:81], v[194:197], v[226:229], v[78:81]
	s_barrier
	s_setprio 0
	s_add_u32 s16, s54, 0x8000
	s_addc_u32 s17, s55, 0
	s_add_i32 s56, s65, s13
	v_lshl_add_u64 v[144:145], s[16:17], 0, v[114:115]
	s_mov_b32 m0, s56
	ds_read_b128 v[198:201], v147 offset:49152
	ds_read_b128 v[202:205], v147 offset:50176
	ds_read_b128 v[206:209], v147 offset:51200
	ds_read_b128 v[210:213], v147 offset:52224
	ds_read_b128 v[214:217], v147 offset:53248
	ds_read_b128 v[218:221], v147 offset:54272
	ds_read_b128 v[222:225], v147 offset:55296
	ds_read_b128 v[226:229], v147 offset:56320
	global_load_lds_dwordx4 v[144:145], off
	s_add_i32 m0, s56, 0x2000
	v_lshl_add_u64 v[144:145], s[16:17], 0, v[136:137]
	s_add_u32 s16, s54, 0x9000
	s_addc_u32 s17, s55, 0
	s_add_i32 s54, s66, s13
	global_load_lds_dwordx4 v[144:145], off
	v_lshl_add_u64 v[144:145], s[16:17], 0, v[114:115]
	s_mov_b32 m0, s54
	s_nop 0
	global_load_lds_dwordx4 v[144:145], off
	v_lshl_add_u64 v[144:145], s[16:17], 0, v[136:137]
	s_add_i32 m0, s54, 0x2000
	s_nop 0
	global_load_lds_dwordx4 v[144:145], off
	v_lshl_add_u64 v[144:145], s[50:51], 0, v[132:133]
	s_mov_b32 m0, s59
	s_nop 0
	global_load_lds_dwordx4 v[144:145], off
	v_lshl_add_u64 v[144:145], s[50:51], 0, v[134:135]
	s_mov_b32 m0, s60
	s_nop 0
	global_load_lds_dwordx4 v[144:145], off
	s_waitcnt vmcnt(8)
	s_waitcnt lgkmcnt(0)
	s_setprio 1
	s_barrier
	v_mfma_f32_16x16x32_bf16 v[50:53], v[148:151], v[198:201], v[50:53]
	v_mfma_f32_16x16x32_bf16 v[62:65], v[158:161], v[198:201], v[62:65]
	v_mfma_f32_16x16x32_bf16 v[34:37], v[148:151], v[206:209], v[34:37]
	v_mfma_f32_16x16x32_bf16 v[38:41], v[158:161], v[206:209], v[38:41]
	v_mfma_f32_16x16x32_bf16 v[18:21], v[148:151], v[214:217], v[18:21]
	v_mfma_f32_16x16x32_bf16 v[26:29], v[158:161], v[214:217], v[26:29]
	v_mfma_f32_16x16x32_bf16 v[2:5], v[148:151], v[222:225], v[2:5]
	v_mfma_f32_16x16x32_bf16 v[6:9], v[158:161], v[222:225], v[6:9]
	v_mfma_f32_16x16x32_bf16 v[50:53], v[152:155], v[202:205], v[50:53]
	v_mfma_f32_16x16x32_bf16 v[62:65], v[166:169], v[202:205], v[62:65]
	v_mfma_f32_16x16x32_bf16 v[34:37], v[152:155], v[210:213], v[34:37]
	v_mfma_f32_16x16x32_bf16 v[38:41], v[166:169], v[210:213], v[38:41]
	v_mfma_f32_16x16x32_bf16 v[18:21], v[152:155], v[218:221], v[18:21]
	v_mfma_f32_16x16x32_bf16 v[26:29], v[166:169], v[218:221], v[26:29]
	v_mfma_f32_16x16x32_bf16 v[2:5], v[152:155], v[226:229], v[2:5]
	v_mfma_f32_16x16x32_bf16 v[6:9], v[166:169], v[226:229], v[6:9]
	s_setprio 0
	s_setprio 1
	v_mfma_f32_16x16x32_bf16 v[54:57], v[170:173], v[198:201], v[54:57]
	v_mfma_f32_16x16x32_bf16 v[66:69], v[178:181], v[198:201], v[66:69]
	v_mfma_f32_16x16x32_bf16 v[42:45], v[170:173], v[206:209], v[42:45]
	v_mfma_f32_16x16x32_bf16 v[46:49], v[178:181], v[206:209], v[46:49]
	v_mfma_f32_16x16x32_bf16 v[22:25], v[170:173], v[214:217], v[22:25]
	v_mfma_f32_16x16x32_bf16 v[30:33], v[178:181], v[214:217], v[30:33]
	v_mfma_f32_16x16x32_bf16 v[10:13], v[170:173], v[222:225], v[10:13]
	v_mfma_f32_16x16x32_bf16 v[14:17], v[178:181], v[222:225], v[14:17]
	v_mfma_f32_16x16x32_bf16 v[54:57], v[174:177], v[202:205], v[54:57]
	v_mfma_f32_16x16x32_bf16 v[66:69], v[194:197], v[202:205], v[66:69]
	v_mfma_f32_16x16x32_bf16 v[42:45], v[174:177], v[210:213], v[42:45]
	v_mfma_f32_16x16x32_bf16 v[46:49], v[194:197], v[210:213], v[46:49]
	v_mfma_f32_16x16x32_bf16 v[22:25], v[174:177], v[218:221], v[22:25]
	v_mfma_f32_16x16x32_bf16 v[30:33], v[194:197], v[218:221], v[30:33]
	v_mfma_f32_16x16x32_bf16 v[10:13], v[174:177], v[226:229], v[10:13]
	v_mfma_f32_16x16x32_bf16 v[14:17], v[194:197], v[226:229], v[14:17]
	s_barrier
	s_setprio 0
	s_add_i32 s64, s64, 2
	s_add_u32 s52, s52, 0x10000
	s_addc_u32 s53, s53, 0
	s_add_u32 s49, s49, 0x10000
	s_addc_u32 s63, s63, 0
	s_cmp_gt_u32 s64, 29
	s_cbranch_scc0 .LBB0_1079
	s_and_b64 vcc, exec, s[10:11]
	s_cbranch_vccz .LBB0_1082
	s_barrier

.Lrx_relu2_w0:
	s_waitcnt vmcnt(24)
	s_waitcnt lgkmcnt(0)
	s_setprio 1
	s_barrier
	v_mfma_f32_16x16x32_bf16 v[128:131], v[148:151], v[198:201], v[128:131]
	v_mfma_f32_16x16x32_bf16 v[124:127], v[158:161], v[198:201], v[124:127]
	v_mfma_f32_16x16x32_bf16 v[110:113], v[148:151], v[206:209], v[110:113]
	v_mfma_f32_16x16x32_bf16 v[106:109], v[158:161], v[206:209], v[106:109]
	v_mfma_f32_16x16x32_bf16 v[94:97], v[148:151], v[214:217], v[94:97]
	v_mfma_f32_16x16x32_bf16 v[90:93], v[158:161], v[214:217], v[90:93]
	v_mfma_f32_16x16x32_bf16 v[78:81], v[148:151], v[222:225], v[78:81]
	v_mfma_f32_16x16x32_bf16 v[74:77], v[158:161], v[222:225], v[74:77]
	v_mfma_f32_16x16x32_bf16 v[128:131], v[152:155], v[202:205], v[128:131]
	v_mfma_f32_16x16x32_bf16 v[124:127], v[166:169], v[202:205], v[124:127]
	v_mfma_f32_16x16x32_bf16 v[110:113], v[152:155], v[210:213], v[110:113]
	v_mfma_f32_16x16x32_bf16 v[106:109], v[166:169], v[210:213], v[106:109]
	v_mfma_f32_16x16x32_bf16 v[94:97], v[152:155], v[218:221], v[94:97]
	v_mfma_f32_16x16x32_bf16 v[90:93], v[166:169], v[218:221], v[90:93]
	v_mfma_f32_16x16x32_bf16 v[78:81], v[152:155], v[226:229], v[78:81]
	v_mfma_f32_16x16x32_bf16 v[74:77], v[166:169], v[226:229], v[74:77]
	s_setprio 0
	s_setprio 1
	v_mfma_f32_16x16x32_bf16 v[120:123], v[170:173], v[198:201], v[120:123]
	v_mfma_f32_16x16x32_bf16 v[116:119], v[178:181], v[198:201], v[116:119]
	v_mfma_f32_16x16x32_bf16 v[102:105], v[170:173], v[206:209], v[102:105]
	v_mfma_f32_16x16x32_bf16 v[98:101], v[178:181], v[206:209], v[98:101]
	v_mfma_f32_16x16x32_bf16 v[86:89], v[170:173], v[214:217], v[86:89]
	v_mfma_f32_16x16x32_bf16 v[82:85], v[178:181], v[214:217], v[82:85]
	v_mfma_f32_16x16x32_bf16 v[70:73], v[170:173], v[222:225], v[70:73]
	v_mfma_f32_16x16x32_bf16 v[66:69], v[178:181], v[222:225], v[66:69]
	v_mfma_f32_16x16x32_bf16 v[120:123], v[174:177], v[202:205], v[120:123]
	v_mfma_f32_16x16x32_bf16 v[116:119], v[194:197], v[202:205], v[116:119]
	v_mfma_f32_16x16x32_bf16 v[102:105], v[174:177], v[210:213], v[102:105]
	v_mfma_f32_16x16x32_bf16 v[98:101], v[194:197], v[210:213], v[98:101]
	v_mfma_f32_16x16x32_bf16 v[86:89], v[174:177], v[218:221], v[86:89]
	v_mfma_f32_16x16x32_bf16 v[82:85], v[194:197], v[218:221], v[82:85]
	v_mfma_f32_16x16x32_bf16 v[70:73], v[174:177], v[226:229], v[70:73]
	v_mfma_f32_16x16x32_bf16 v[66:69], v[194:197], v[226:229], v[66:69]
	s_barrier
	s_setprio 0
	s_add_i32 s16, s16, s7
	v_lshl_add_u64 v[144:145], s[50:51], 0, v[114:115]
	s_mov_b32 m0, s16
	ds_read_b128 v[198:201], v147 offset:16384
	ds_read_b128 v[202:205], v147 offset:17408
	ds_read_b128 v[206:209], v147 offset:18432
	ds_read_b128 v[210:213], v147 offset:19456
	ds_read_b128 v[214:217], v147 offset:20480
	ds_read_b128 v[218:221], v147 offset:21504
	ds_read_b128 v[222:225], v147 offset:22528
	ds_read_b128 v[226:229], v147 offset:23552
	global_load_lds_dwordx4 v[144:145], off
	s_add_i32 m0, s16, 0x2000
	s_add_u32 s16, s50, 0x1000
	v_lshl_add_u64 v[144:145], s[50:51], 0, v[136:137]
	s_addc_u32 s17, s51, 0
	s_add_i32 s65, s65, s7
	global_load_lds_dwordx4 v[144:145], off
	v_lshl_add_u64 v[144:145], s[16:17], 0, v[114:115]
	s_mov_b32 m0, s65
	s_nop 0
	global_load_lds_dwordx4 v[144:145], off
	v_lshl_add_u64 v[144:145], s[16:17], 0, v[136:137]
	s_add_i32 m0, s65, 0x2000
	s_nop 0
	global_load_lds_dwordx4 v[144:145], off
	v_lshl_add_u64 v[144:145], s[52:53], 0, v[132:133]
	s_mov_b32 m0, s20
	s_nop 0
	global_load_lds_dwordx4 v[144:145], off
	v_lshl_add_u64 v[144:145], s[52:53], 0, v[134:135]
	s_mov_b32 m0, s21
	s_nop 0
	global_load_lds_dwordx4 v[144:145], off
	s_cmp_lg_u32 s32, 0
	s_cbranch_scc1 .Lrx_relu2_w1
	s_waitcnt vmcnt(8)
.Lrx_relu2_w1:
	s_waitcnt vmcnt(24)
	s_waitcnt lgkmcnt(0)
	s_setprio 1
	s_barrier
	v_mfma_f32_16x16x32_bf16 v[62:65], v[148:151], v[198:201], v[62:65]
	v_mfma_f32_16x16x32_bf16 v[58:61], v[158:161], v[198:201], v[58:61]
	v_mfma_f32_16x16x32_bf16 v[46:49], v[148:151], v[206:209], v[46:49]
	v_mfma_f32_16x16x32_bf16 v[42:45], v[158:161], v[206:209], v[42:45]
	v_mfma_f32_16x16x32_bf16 v[30:33], v[148:151], v[214:217], v[30:33]
	v_mfma_f32_16x16x32_bf16 v[26:29], v[158:161], v[214:217], v[26:29]
	v_mfma_f32_16x16x32_bf16 v[14:17], v[148:151], v[222:225], v[14:17]
	v_mfma_f32_16x16x32_bf16 v[10:13], v[158:161], v[222:225], v[10:13]
	v_mfma_f32_16x16x32_bf16 v[62:65], v[152:155], v[202:205], v[62:65]
	v_mfma_f32_16x16x32_bf16 v[58:61], v[166:169], v[202:205], v[58:61]
	v_mfma_f32_16x16x32_bf16 v[46:49], v[152:155], v[210:213], v[46:49]
	v_mfma_f32_16x16x32_bf16 v[42:45], v[166:169], v[210:213], v[42:45]
	v_mfma_f32_16x16x32_bf16 v[30:33], v[152:155], v[218:221], v[30:33]
	v_mfma_f32_16x16x32_bf16 v[26:29], v[166:169], v[218:221], v[26:29]
	v_mfma_f32_16x16x32_bf16 v[14:17], v[152:155], v[226:229], v[14:17]
	v_mfma_f32_16x16x32_bf16 v[10:13], v[166:169], v[226:229], v[10:13]
	s_setprio 0
	s_setprio 1
	v_mfma_f32_16x16x32_bf16 v[54:57], v[170:173], v[198:201], v[54:57]
	v_mfma_f32_16x16x32_bf16 v[50:53], v[178:181], v[198:201], v[50:53]
	v_mfma_f32_16x16x32_bf16 v[38:41], v[170:173], v[206:209], v[38:41]
	v_mfma_f32_16x16x32_bf16 v[34:37], v[178:181], v[206:209], v[34:37]
	v_mfma_f32_16x16x32_bf16 v[22:25], v[170:173], v[214:217], v[22:25]
	v_mfma_f32_16x16x32_bf16 v[18:21], v[178:181], v[214:217], v[18:21]
	v_mfma_f32_16x16x32_bf16 v[6:9], v[170:173], v[222:225], v[6:9]
	v_mfma_f32_16x16x32_bf16 v[2:5], v[178:181], v[222:225], v[2:5]
	v_mfma_f32_16x16x32_bf16 v[54:57], v[174:177], v[202:205], v[54:57]
	v_mfma_f32_16x16x32_bf16 v[50:53], v[194:197], v[202:205], v[50:53]
	v_mfma_f32_16x16x32_bf16 v[38:41], v[174:177], v[210:213], v[38:41]
	v_mfma_f32_16x16x32_bf16 v[34:37], v[194:197], v[210:213], v[34:37]
	v_mfma_f32_16x16x32_bf16 v[22:25], v[174:177], v[218:221], v[22:25]
	v_mfma_f32_16x16x32_bf16 v[18:21], v[194:197], v[218:221], v[18:21]
	v_mfma_f32_16x16x32_bf16 v[6:9], v[174:177], v[226:229], v[6:9]
	v_mfma_f32_16x16x32_bf16 v[2:5], v[194:197], v[226:229], v[2:5]
	s_barrier
	s_setprio 0
	s_add_i32 s65, 0, 0x18000
	v_add_u32_e32 v144, s65, v1
	s_add_i32 s66, 0, 0x1c000
	ds_read_b128 v[148:151], v144
	ds_read_b128 v[152:155], v144 offset:1024
	ds_read_b128 v[158:161], v144 offset:2048
	ds_read_b128 v[166:169], v144 offset:3072
	v_add_u32_e32 v144, s66, v1
	ds_read_b128 v[170:173], v144
	ds_read_b128 v[174:177], v144 offset:1024
	ds_read_b128 v[178:181], v144 offset:2048
	ds_read_b128 v[194:197], v144 offset:3072
	s_add_u32 s16, s52, 0x4000
	s_addc_u32 s17, s53, 0
	s_mov_b32 m0, s24
	v_lshl_add_u64 v[144:145], s[16:17], 0, v[132:133]
	ds_read_b128 v[198:201], v147 offset:32768
	ds_read_b128 v[202:205], v147 offset:33792
	ds_read_b128 v[206:209], v147 offset:34816
	ds_read_b128 v[210:213], v147 offset:35840
	ds_read_b128 v[214:217], v147 offset:36864
	ds_read_b128 v[218:221], v147 offset:37888
	ds_read_b128 v[222:225], v147 offset:38912
	ds_read_b128 v[226:229], v147 offset:39936
	global_load_lds_dwordx4 v[144:145], off
	v_lshl_add_u64 v[144:145], s[16:17], 0, v[134:135]
	s_mov_b32 m0, s37
	s_nop 0
	global_load_lds_dwordx4 v[144:145], off
	s_cmp_lg_u32 s32, 0
	s_cbranch_scc1 .Lrx_relu2_w2
	s_waitcnt vmcnt(8)
.Lrx_relu2_w2:
	s_waitcnt vmcnt(24)
	s_mov_b32 s32, 0
	s_waitcnt lgkmcnt(0)
	s_setprio 1
	s_barrier
	v_mfma_f32_16x16x32_bf16 v[128:131], v[148:151], v[198:201], v[128:131]
	v_mfma_f32_16x16x32_bf16 v[124:127], v[158:161], v[198:201], v[124:127]
	v_mfma_f32_16x16x32_bf16 v[110:113], v[148:151], v[206:209], v[110:113]
	v_mfma_f32_16x16x32_bf16 v[106:109], v[158:161], v[206:209], v[106:109]
	v_mfma_f32_16x16x32_bf16 v[94:97], v[148:151], v[214:217], v[94:97]
	v_mfma_f32_16x16x32_bf16 v[90:93], v[158:161], v[214:217], v[90:93]
	v_mfma_f32_16x16x32_bf16 v[78:81], v[148:151], v[222:225], v[78:81]
	v_mfma_f32_16x16x32_bf16 v[74:77], v[158:161], v[222:225], v[74:77]
	v_mfma_f32_16x16x32_bf16 v[128:131], v[152:155], v[202:205], v[128:131]
	v_mfma_f32_16x16x32_bf16 v[124:127], v[166:169], v[202:205], v[124:127]
	v_mfma_f32_16x16x32_bf16 v[110:113], v[152:155], v[210:213], v[110:113]
	v_mfma_f32_16x16x32_bf16 v[106:109], v[166:169], v[210:213], v[106:109]
	v_mfma_f32_16x16x32_bf16 v[94:97], v[152:155], v[218:221], v[94:97]
	v_mfma_f32_16x16x32_bf16 v[90:93], v[166:169], v[218:221], v[90:93]
	v_mfma_f32_16x16x32_bf16 v[78:81], v[152:155], v[226:229], v[78:81]
	v_mfma_f32_16x16x32_bf16 v[74:77], v[166:169], v[226:229], v[74:77]
	s_setprio 0
	s_setprio 1
	v_mfma_f32_16x16x32_bf16 v[120:123], v[170:173], v[198:201], v[120:123]
	v_mfma_f32_16x16x32_bf16 v[116:119], v[178:181], v[198:201], v[116:119]
	v_mfma_f32_16x16x32_bf16 v[102:105], v[170:173], v[206:209], v[102:105]
	v_mfma_f32_16x16x32_bf16 v[98:101], v[178:181], v[206:209], v[98:101]
	v_mfma_f32_16x16x32_bf16 v[86:89], v[170:173], v[214:217], v[86:89]
	v_mfma_f32_16x16x32_bf16 v[82:85], v[178:181], v[214:217], v[82:85]
	v_mfma_f32_16x16x32_bf16 v[70:73], v[170:173], v[222:225], v[70:73]
	v_mfma_f32_16x16x32_bf16 v[66:69], v[178:181], v[222:225], v[66:69]
	v_mfma_f32_16x16x32_bf16 v[120:123], v[174:177], v[202:205], v[120:123]
	v_mfma_f32_16x16x32_bf16 v[116:119], v[194:197], v[202:205], v[116:119]
	v_mfma_f32_16x16x32_bf16 v[102:105], v[174:177], v[210:213], v[102:105]
	v_mfma_f32_16x16x32_bf16 v[98:101], v[194:197], v[210:213], v[98:101]
	v_mfma_f32_16x16x32_bf16 v[86:89], v[174:177], v[218:221], v[86:89]
	v_mfma_f32_16x16x32_bf16 v[82:85], v[194:197], v[218:221], v[82:85]
	v_mfma_f32_16x16x32_bf16 v[70:73], v[174:177], v[226:229], v[70:73]
	v_mfma_f32_16x16x32_bf16 v[66:69], v[194:197], v[226:229], v[66:69]
	s_barrier
	s_setprio 0
	s_add_u32 s16, s50, 0x8000
	s_addc_u32 s17, s51, 0
	s_add_i32 s52, s65, s7
	v_lshl_add_u64 v[144:145], s[16:17], 0, v[114:115]
	s_mov_b32 m0, s52
	ds_read_b128 v[198:201], v147 offset:49152
	ds_read_b128 v[202:205], v147 offset:50176
	ds_read_b128 v[206:209], v147 offset:51200
	ds_read_b128 v[210:213], v147 offset:52224
	ds_read_b128 v[214:217], v147 offset:53248
	ds_read_b128 v[218:221], v147 offset:54272
	ds_read_b128 v[222:225], v147 offset:55296
	ds_read_b128 v[226:229], v147 offset:56320
	global_load_lds_dwordx4 v[144:145], off
	s_add_i32 m0, s52, 0x2000
	v_lshl_add_u64 v[144:145], s[16:17], 0, v[136:137]
	s_add_u32 s16, s50, 0x9000
	s_addc_u32 s17, s51, 0
	s_add_i32 s50, s66, s7
	global_load_lds_dwordx4 v[144:145], off
	v_lshl_add_u64 v[144:145], s[16:17], 0, v[114:115]
	s_mov_b32 m0, s50
	s_nop 0
	global_load_lds_dwordx4 v[144:145], off
	v_lshl_add_u64 v[144:145], s[16:17], 0, v[136:137]
	s_add_i32 m0, s50, 0x2000
	s_nop 0
	global_load_lds_dwordx4 v[144:145], off
	v_lshl_add_u64 v[144:145], s[48:49], 0, v[132:133]
	s_mov_b32 m0, s54
	s_nop 0
	global_load_lds_dwordx4 v[144:145], off
	v_lshl_add_u64 v[144:145], s[48:49], 0, v[134:135]
	s_mov_b32 m0, s55
	s_nop 0
	global_load_lds_dwordx4 v[144:145], off
	s_waitcnt vmcnt(8)
	s_waitcnt lgkmcnt(0)
	s_setprio 1
	s_barrier
	v_mfma_f32_16x16x32_bf16 v[62:65], v[148:151], v[198:201], v[62:65]
	v_mfma_f32_16x16x32_bf16 v[58:61], v[158:161], v[198:201], v[58:61]
	v_mfma_f32_16x16x32_bf16 v[46:49], v[148:151], v[206:209], v[46:49]
	v_mfma_f32_16x16x32_bf16 v[42:45], v[158:161], v[206:209], v[42:45]
	v_mfma_f32_16x16x32_bf16 v[30:33], v[148:151], v[214:217], v[30:33]
	v_mfma_f32_16x16x32_bf16 v[26:29], v[158:161], v[214:217], v[26:29]
	v_mfma_f32_16x16x32_bf16 v[14:17], v[148:151], v[222:225], v[14:17]
	v_mfma_f32_16x16x32_bf16 v[10:13], v[158:161], v[222:225], v[10:13]
	v_mfma_f32_16x16x32_bf16 v[62:65], v[152:155], v[202:205], v[62:65]
	v_mfma_f32_16x16x32_bf16 v[58:61], v[166:169], v[202:205], v[58:61]
	v_mfma_f32_16x16x32_bf16 v[46:49], v[152:155], v[210:213], v[46:49]
	v_mfma_f32_16x16x32_bf16 v[42:45], v[166:169], v[210:213], v[42:45]
	v_mfma_f32_16x16x32_bf16 v[30:33], v[152:155], v[218:221], v[30:33]
	v_mfma_f32_16x16x32_bf16 v[26:29], v[166:169], v[218:221], v[26:29]
	v_mfma_f32_16x16x32_bf16 v[14:17], v[152:155], v[226:229], v[14:17]
	v_mfma_f32_16x16x32_bf16 v[10:13], v[166:169], v[226:229], v[10:13]
	s_setprio 0
	s_setprio 1
	v_mfma_f32_16x16x32_bf16 v[54:57], v[170:173], v[198:201], v[54:57]
	v_mfma_f32_16x16x32_bf16 v[50:53], v[178:181], v[198:201], v[50:53]
	v_mfma_f32_16x16x32_bf16 v[38:41], v[170:173], v[206:209], v[38:41]
	v_mfma_f32_16x16x32_bf16 v[34:37], v[178:181], v[206:209], v[34:37]
	v_mfma_f32_16x16x32_bf16 v[22:25], v[170:173], v[214:217], v[22:25]
	v_mfma_f32_16x16x32_bf16 v[18:21], v[178:181], v[214:217], v[18:21]
	v_mfma_f32_16x16x32_bf16 v[6:9], v[170:173], v[222:225], v[6:9]
	v_mfma_f32_16x16x32_bf16 v[2:5], v[178:181], v[222:225], v[2:5]
	v_mfma_f32_16x16x32_bf16 v[54:57], v[174:177], v[202:205], v[54:57]
	v_mfma_f32_16x16x32_bf16 v[50:53], v[194:197], v[202:205], v[50:53]
	v_mfma_f32_16x16x32_bf16 v[38:41], v[174:177], v[210:213], v[38:41]
	v_mfma_f32_16x16x32_bf16 v[34:37], v[194:197], v[210:213], v[34:37]
	v_mfma_f32_16x16x32_bf16 v[22:25], v[174:177], v[218:221], v[22:25]
	v_mfma_f32_16x16x32_bf16 v[18:21], v[194:197], v[218:221], v[18:21]
	v_mfma_f32_16x16x32_bf16 v[6:9], v[174:177], v[226:229], v[6:9]
	v_mfma_f32_16x16x32_bf16 v[2:5], v[194:197], v[226:229], v[2:5]
	s_barrier
	s_setprio 0
	s_add_i32 s64, s64, 2
	s_add_u32 s46, s46, 0x10000
	s_addc_u32 s47, s47, 0
	s_add_u32 s62, s62, 0x10000
	s_addc_u32 s63, s63, 0
	s_cmp_gt_u32 s64, 29
	s_cbranch_scc0 .LBB0_1230
	s_add_u32 s100, s60, 0xc000
	s_addc_u32 s101, s29, 0
	v_lshl_add_u64 v[144:145], s[100:101], 0, v[140:141]
	s_add_i32 m0, s20, 0xc000
	s_nop 0
	global_load_lds_dwordx4 v[144:145], off
	v_lshl_add_u64 v[144:145], s[100:101], 0, v[142:143]
	s_add_i32 m0, s20, 0xe000
	s_nop 0
	global_load_lds_dwordx4 v[144:145], off
	s_and_b64 vcc, exec, s[10:11]
	s_cbranch_vccz .LBB0_1233
	s_barrier

.LBB0_1334:
	s_add_u32 s16, s52, 0x4000
	s_addc_u32 s17, s53, 0
	s_cmpk_eq_i32 s66, 0x7c
	s_cselect_b32 s56, s29, s16
	s_cselect_b32 s57, s24, s17
	s_cselect_b32 s55, s27, s65
	s_cselect_b32 s54, s47, s49
	s_add_u32 s50, s56, 0x8000
	s_addc_u32 s51, s57, 0
	s_add_i32 s16, 0, 0x10000
	v_add_u32_e32 v144, s16, v146
	s_add_i32 s67, 0, 0x14000
	ds_read_b128 v[148:151], v144
	ds_read_b128 v[152:155], v144 offset:1024
	ds_read_b128 v[158:161], v144 offset:2048
	ds_read_b128 v[166:169], v144 offset:3072
	v_add_u32_e32 v144, s67, v146
	ds_read_b128 v[170:173], v144
	ds_read_b128 v[174:177], v144 offset:1024
	ds_read_b128 v[178:181], v144 offset:2048
	ds_read_b128 v[194:197], v144 offset:3072
	v_lshl_add_u64 v[144:145], s[52:53], 0, v[140:141]
	s_add_i32 m0, s37, 0xc000
	ds_read_b128 v[198:201], v147
	ds_read_b128 v[202:205], v147 offset:1024
	ds_read_b128 v[206:209], v147 offset:2048
	ds_read_b128 v[210:213], v147 offset:3072
	ds_read_b128 v[214:217], v147 offset:4096
	ds_read_b128 v[218:221], v147 offset:5120
	ds_read_b128 v[222:225], v147 offset:6144
	ds_read_b128 v[226:229], v147 offset:7168
	global_load_lds_dwordx4 v[144:145], off
	v_lshl_add_u64 v[144:145], s[52:53], 0, v[142:143]
	s_add_i32 m0, s37, 0xe000
	s_nop 0
	global_load_lds_dwordx4 v[144:145], off
	s_waitcnt vmcnt(8)
	s_waitcnt lgkmcnt(0)
	s_setprio 1
	s_barrier
	v_mfma_f32_16x16x32_bf16 v[116:119], v[148:151], v[198:201], v[116:119]
	v_mfma_f32_16x16x32_bf16 v[124:127], v[158:161], v[198:201], v[124:127]
	v_mfma_f32_16x16x32_bf16 v[98:101], v[148:151], v[206:209], v[98:101]
	v_mfma_f32_16x16x32_bf16 v[102:105], v[158:161], v[206:209], v[102:105]
	v_mfma_f32_16x16x32_bf16 v[82:85], v[148:151], v[214:217], v[82:85]
	v_mfma_f32_16x16x32_bf16 v[90:93], v[158:161], v[214:217], v[90:93]
	v_mfma_f32_16x16x32_bf16 v[58:61], v[148:151], v[222:225], v[58:61]
	v_mfma_f32_16x16x32_bf16 v[70:73], v[158:161], v[222:225], v[70:73]
	v_mfma_f32_16x16x32_bf16 v[116:119], v[152:155], v[202:205], v[116:119]
	v_mfma_f32_16x16x32_bf16 v[124:127], v[166:169], v[202:205], v[124:127]
	v_mfma_f32_16x16x32_bf16 v[98:101], v[152:155], v[210:213], v[98:101]
	v_mfma_f32_16x16x32_bf16 v[102:105], v[166:169], v[210:213], v[102:105]
	v_mfma_f32_16x16x32_bf16 v[82:85], v[152:155], v[218:221], v[82:85]
	v_mfma_f32_16x16x32_bf16 v[90:93], v[166:169], v[218:221], v[90:93]
	v_mfma_f32_16x16x32_bf16 v[58:61], v[152:155], v[226:229], v[58:61]
	v_mfma_f32_16x16x32_bf16 v[70:73], v[166:169], v[226:229], v[70:73]
	s_setprio 0
	s_setprio 1
	v_mfma_f32_16x16x32_bf16 v[120:123], v[170:173], v[198:201], v[120:123]
	v_mfma_f32_16x16x32_bf16 v[128:131], v[178:181], v[198:201], v[128:131]
	v_mfma_f32_16x16x32_bf16 v[106:109], v[170:173], v[206:209], v[106:109]
	v_mfma_f32_16x16x32_bf16 v[110:113], v[178:181], v[206:209], v[110:113]
	v_mfma_f32_16x16x32_bf16 v[86:89], v[170:173], v[214:217], v[86:89]
	v_mfma_f32_16x16x32_bf16 v[94:97], v[178:181], v[214:217], v[94:97]
	v_mfma_f32_16x16x32_bf16 v[74:77], v[170:173], v[222:225], v[74:77]
	v_mfma_f32_16x16x32_bf16 v[78:81], v[178:181], v[222:225], v[78:81]
	v_mfma_f32_16x16x32_bf16 v[120:123], v[174:177], v[202:205], v[120:123]
	v_mfma_f32_16x16x32_bf16 v[128:131], v[194:197], v[202:205], v[128:131]
	v_mfma_f32_16x16x32_bf16 v[106:109], v[174:177], v[210:213], v[106:109]
	v_mfma_f32_16x16x32_bf16 v[110:113], v[194:197], v[210:213], v[110:113]
	v_mfma_f32_16x16x32_bf16 v[86:89], v[174:177], v[218:221], v[86:89]
	v_mfma_f32_16x16x32_bf16 v[94:97], v[194:197], v[218:221], v[94:97]
	v_mfma_f32_16x16x32_bf16 v[74:77], v[174:177], v[226:229], v[74:77]
	v_mfma_f32_16x16x32_bf16 v[78:81], v[194:197], v[226:229], v[78:81]
	s_barrier
	s_setprio 0
	s_add_i32 s16, s16, s15
	v_lshl_add_u64 v[144:145], s[54:55], 0, v[114:115]
	s_mov_b32 m0, s16
	ds_read_b128 v[198:201], v147 offset:16384
	ds_read_b128 v[202:205], v147 offset:17408
	ds_read_b128 v[206:209], v147 offset:18432
	ds_read_b128 v[210:213], v147 offset:19456
	ds_read_b128 v[214:217], v147 offset:20480
	ds_read_b128 v[218:221], v147 offset:21504
	ds_read_b128 v[222:225], v147 offset:22528
	ds_read_b128 v[226:229], v147 offset:23552
	global_load_lds_dwordx4 v[144:145], off
	s_add_i32 m0, s16, 0x2000
	s_add_u32 s16, s54, 0x1000
	v_lshl_add_u64 v[144:145], s[54:55], 0, v[136:137]
	s_addc_u32 s17, s55, 0
	s_add_i32 s67, s67, s15
	global_load_lds_dwordx4 v[144:145], off
	v_lshl_add_u64 v[144:145], s[16:17], 0, v[114:115]
	s_mov_b32 m0, s67
	s_nop 0
	global_load_lds_dwordx4 v[144:145], off
	v_lshl_add_u64 v[144:145], s[16:17], 0, v[136:137]
	s_add_i32 m0, s67, 0x2000
	s_nop 0
	global_load_lds_dwordx4 v[144:145], off
	v_lshl_add_u64 v[144:145], s[56:57], 0, v[132:133]
	s_mov_b32 m0, s37
	s_nop 0
	global_load_lds_dwordx4 v[144:145], off
	v_lshl_add_u64 v[144:145], s[56:57], 0, v[134:135]
	s_mov_b32 m0, s58
	s_nop 0
	global_load_lds_dwordx4 v[144:145], off
	s_waitcnt vmcnt(8)
	s_waitcnt lgkmcnt(0)
	s_setprio 1
	s_barrier
	v_mfma_f32_16x16x32_bf16 v[50:53], v[148:151], v[198:201], v[50:53]
	v_mfma_f32_16x16x32_bf16 v[62:65], v[158:161], v[198:201], v[62:65]
	v_mfma_f32_16x16x32_bf16 v[34:37], v[148:151], v[206:209], v[34:37]
	v_mfma_f32_16x16x32_bf16 v[38:41], v[158:161], v[206:209], v[38:41]
	v_mfma_f32_16x16x32_bf16 v[18:21], v[148:151], v[214:217], v[18:21]
	v_mfma_f32_16x16x32_bf16 v[26:29], v[158:161], v[214:217], v[26:29]
	v_mfma_f32_16x16x32_bf16 v[2:5], v[148:151], v[222:225], v[2:5]
	v_mfma_f32_16x16x32_bf16 v[6:9], v[158:161], v[222:225], v[6:9]
	v_mfma_f32_16x16x32_bf16 v[50:53], v[152:155], v[202:205], v[50:53]
	v_mfma_f32_16x16x32_bf16 v[62:65], v[166:169], v[202:205], v[62:65]
	v_mfma_f32_16x16x32_bf16 v[34:37], v[152:155], v[210:213], v[34:37]
	v_mfma_f32_16x16x32_bf16 v[38:41], v[166:169], v[210:213], v[38:41]
	v_mfma_f32_16x16x32_bf16 v[18:21], v[152:155], v[218:221], v[18:21]
	v_mfma_f32_16x16x32_bf16 v[26:29], v[166:169], v[218:221], v[26:29]
	v_mfma_f32_16x16x32_bf16 v[2:5], v[152:155], v[226:229], v[2:5]
	v_mfma_f32_16x16x32_bf16 v[6:9], v[166:169], v[226:229], v[6:9]
	s_setprio 0
	s_setprio 1
	v_mfma_f32_16x16x32_bf16 v[54:57], v[170:173], v[198:201], v[54:57]
	v_mfma_f32_16x16x32_bf16 v[66:69], v[178:181], v[198:201], v[66:69]
	v_mfma_f32_16x16x32_bf16 v[42:45], v[170:173], v[206:209], v[42:45]
	v_mfma_f32_16x16x32_bf16 v[46:49], v[178:181], v[206:209], v[46:49]
	v_mfma_f32_16x16x32_bf16 v[22:25], v[170:173], v[214:217], v[22:25]
	v_mfma_f32_16x16x32_bf16 v[30:33], v[178:181], v[214:217], v[30:33]
	v_mfma_f32_16x16x32_bf16 v[10:13], v[170:173], v[222:225], v[10:13]
	v_mfma_f32_16x16x32_bf16 v[14:17], v[178:181], v[222:225], v[14:17]
	v_mfma_f32_16x16x32_bf16 v[54:57], v[174:177], v[202:205], v[54:57]
	v_mfma_f32_16x16x32_bf16 v[66:69], v[194:197], v[202:205], v[66:69]
	v_mfma_f32_16x16x32_bf16 v[42:45], v[174:177], v[210:213], v[42:45]
	v_mfma_f32_16x16x32_bf16 v[46:49], v[194:197], v[210:213], v[46:49]
	v_mfma_f32_16x16x32_bf16 v[22:25], v[174:177], v[218:221], v[22:25]
	v_mfma_f32_16x16x32_bf16 v[30:33], v[194:197], v[218:221], v[30:33]
	v_mfma_f32_16x16x32_bf16 v[10:13], v[174:177], v[226:229], v[10:13]
	v_mfma_f32_16x16x32_bf16 v[14:17], v[194:197], v[226:229], v[14:17]
	s_barrier
	s_setprio 0
	s_add_i32 s67, 0, 0x18000
	v_add_u32_e32 v144, s67, v146
	s_add_i32 s68, 0, 0x1c000
	ds_read_b128 v[148:151], v144
	ds_read_b128 v[152:155], v144 offset:1024
	ds_read_b128 v[158:161], v144 offset:2048
	ds_read_b128 v[166:169], v144 offset:3072
	v_add_u32_e32 v144, s68, v146
	ds_read_b128 v[170:173], v144
	ds_read_b128 v[174:177], v144 offset:1024
	ds_read_b128 v[178:181], v144 offset:2048
	ds_read_b128 v[194:197], v144 offset:3072
	s_add_u32 s16, s56, 0x4000
	s_addc_u32 s17, s57, 0
	s_mov_b32 m0, s59
	v_lshl_add_u64 v[144:145], s[16:17], 0, v[132:133]
	ds_read_b128 v[198:201], v147 offset:32768
	ds_read_b128 v[202:205], v147 offset:33792
	ds_read_b128 v[206:209], v147 offset:34816
	ds_read_b128 v[210:213], v147 offset:35840
	ds_read_b128 v[214:217], v147 offset:36864
	ds_read_b128 v[218:221], v147 offset:37888
	ds_read_b128 v[222:225], v147 offset:38912
	ds_read_b128 v[226:229], v147 offset:39936
	global_load_lds_dwordx4 v[144:145], off
	v_lshl_add_u64 v[144:145], s[16:17], 0, v[134:135]
	s_mov_b32 m0, s60
	s_nop 0
	global_load_lds_dwordx4 v[144:145], off
	s_waitcnt vmcnt(8)
	s_waitcnt lgkmcnt(0)
	s_setprio 1
	s_barrier
	v_mfma_f32_16x16x32_bf16 v[116:119], v[148:151], v[198:201], v[116:119]
	v_mfma_f32_16x16x32_bf16 v[124:127], v[158:161], v[198:201], v[124:127]
	v_mfma_f32_16x16x32_bf16 v[98:101], v[148:151], v[206:209], v[98:101]
	v_mfma_f32_16x16x32_bf16 v[102:105], v[158:161], v[206:209], v[102:105]
	v_mfma_f32_16x16x32_bf16 v[82:85], v[148:151], v[214:217], v[82:85]
	v_mfma_f32_16x16x32_bf16 v[90:93], v[158:161], v[214:217], v[90:93]
	v_mfma_f32_16x16x32_bf16 v[58:61], v[148:151], v[222:225], v[58:61]
	v_mfma_f32_16x16x32_bf16 v[70:73], v[158:161], v[222:225], v[70:73]
	v_mfma_f32_16x16x32_bf16 v[116:119], v[152:155], v[202:205], v[116:119]
	v_mfma_f32_16x16x32_bf16 v[124:127], v[166:169], v[202:205], v[124:127]
	v_mfma_f32_16x16x32_bf16 v[98:101], v[152:155], v[210:213], v[98:101]
	v_mfma_f32_16x16x32_bf16 v[102:105], v[166:169], v[210:213], v[102:105]
	v_mfma_f32_16x16x32_bf16 v[82:85], v[152:155], v[218:221], v[82:85]
	v_mfma_f32_16x16x32_bf16 v[90:93], v[166:169], v[218:221], v[90:93]
	v_mfma_f32_16x16x32_bf16 v[58:61], v[152:155], v[226:229], v[58:61]
	v_mfma_f32_16x16x32_bf16 v[70:73], v[166:169], v[226:229], v[70:73]
	s_setprio 0
	s_setprio 1
	v_mfma_f32_16x16x32_bf16 v[120:123], v[170:173], v[198:201], v[120:123]
	v_mfma_f32_16x16x32_bf16 v[128:131], v[178:181], v[198:201], v[128:131]
	v_mfma_f32_16x16x32_bf16 v[106:109], v[170:173], v[206:209], v[106:109]
	v_mfma_f32_16x16x32_bf16 v[110:113], v[178:181], v[206:209], v[110:113]
	v_mfma_f32_16x16x32_bf16 v[86:89], v[170:173], v[214:217], v[86:89]
	v_mfma_f32_16x16x32_bf16 v[94:97], v[178:181], v[214:217], v[94:97]
	v_mfma_f32_16x16x32_bf16 v[74:77], v[170:173], v[222:225], v[74:77]
	v_mfma_f32_16x16x32_bf16 v[78:81], v[178:181], v[222:225], v[78:81]
	v_mfma_f32_16x16x32_bf16 v[120:123], v[174:177], v[202:205], v[120:123]
	v_mfma_f32_16x16x32_bf16 v[128:131], v[194:197], v[202:205], v[128:131]
	v_mfma_f32_16x16x32_bf16 v[106:109], v[174:177], v[210:213], v[106:109]
	v_mfma_f32_16x16x32_bf16 v[110:113], v[194:197], v[210:213], v[110:113]
	v_mfma_f32_16x16x32_bf16 v[86:89], v[174:177], v[218:221], v[86:89]
	v_mfma_f32_16x16x32_bf16 v[94:97], v[194:197], v[218:221], v[94:97]
	v_mfma_f32_16x16x32_bf16 v[74:77], v[174:177], v[226:229], v[74:77]
	v_mfma_f32_16x16x32_bf16 v[78:81], v[194:197], v[226:229], v[78:81]
	s_barrier
	s_setprio 0
	s_add_u32 s16, s54, 0x8000
	s_addc_u32 s17, s55, 0
	s_add_i32 s56, s67, s15
	v_lshl_add_u64 v[144:145], s[16:17], 0, v[114:115]
	s_mov_b32 m0, s56
	ds_read_b128 v[198:201], v147 offset:49152
	ds_read_b128 v[202:205], v147 offset:50176
	ds_read_b128 v[206:209], v147 offset:51200
	ds_read_b128 v[210:213], v147 offset:52224
	ds_read_b128 v[214:217], v147 offset:53248
	ds_read_b128 v[218:221], v147 offset:54272
	ds_read_b128 v[222:225], v147 offset:55296
	ds_read_b128 v[226:229], v147 offset:56320
	global_load_lds_dwordx4 v[144:145], off
	s_add_i32 m0, s56, 0x2000
	v_lshl_add_u64 v[144:145], s[16:17], 0, v[136:137]
	s_add_u32 s16, s54, 0x9000
	s_addc_u32 s17, s55, 0
	s_add_i32 s54, s68, s15
	global_load_lds_dwordx4 v[144:145], off
	v_lshl_add_u64 v[144:145], s[16:17], 0, v[114:115]
	s_mov_b32 m0, s54
	s_nop 0
	global_load_lds_dwordx4 v[144:145], off
	v_lshl_add_u64 v[144:145], s[16:17], 0, v[136:137]
	s_add_i32 m0, s54, 0x2000
	s_nop 0
	global_load_lds_dwordx4 v[144:145], off
	v_lshl_add_u64 v[144:145], s[50:51], 0, v[132:133]
	s_mov_b32 m0, s61
	s_nop 0
	global_load_lds_dwordx4 v[144:145], off
	v_lshl_add_u64 v[144:145], s[50:51], 0, v[134:135]
	s_mov_b32 m0, s62
	s_nop 0
	global_load_lds_dwordx4 v[144:145], off
	s_waitcnt vmcnt(8)
	s_waitcnt lgkmcnt(0)
	s_setprio 1
	s_barrier
	v_mfma_f32_16x16x32_bf16 v[50:53], v[148:151], v[198:201], v[50:53]
	v_mfma_f32_16x16x32_bf16 v[62:65], v[158:161], v[198:201], v[62:65]
	v_mfma_f32_16x16x32_bf16 v[34:37], v[148:151], v[206:209], v[34:37]
	v_mfma_f32_16x16x32_bf16 v[38:41], v[158:161], v[206:209], v[38:41]
	v_mfma_f32_16x16x32_bf16 v[18:21], v[148:151], v[214:217], v[18:21]
	v_mfma_f32_16x16x32_bf16 v[26:29], v[158:161], v[214:217], v[26:29]
	v_mfma_f32_16x16x32_bf16 v[2:5], v[148:151], v[222:225], v[2:5]
	v_mfma_f32_16x16x32_bf16 v[6:9], v[158:161], v[222:225], v[6:9]
	v_mfma_f32_16x16x32_bf16 v[50:53], v[152:155], v[202:205], v[50:53]
	v_mfma_f32_16x16x32_bf16 v[62:65], v[166:169], v[202:205], v[62:65]
	v_mfma_f32_16x16x32_bf16 v[34:37], v[152:155], v[210:213], v[34:37]
	v_mfma_f32_16x16x32_bf16 v[38:41], v[166:169], v[210:213], v[38:41]
	v_mfma_f32_16x16x32_bf16 v[18:21], v[152:155], v[218:221], v[18:21]
	v_mfma_f32_16x16x32_bf16 v[26:29], v[166:169], v[218:221], v[26:29]
	v_mfma_f32_16x16x32_bf16 v[2:5], v[152:155], v[226:229], v[2:5]
	v_mfma_f32_16x16x32_bf16 v[6:9], v[166:169], v[226:229], v[6:9]
	s_setprio 0
	s_setprio 1
	v_mfma_f32_16x16x32_bf16 v[54:57], v[170:173], v[198:201], v[54:57]
	v_mfma_f32_16x16x32_bf16 v[66:69], v[178:181], v[198:201], v[66:69]
	v_mfma_f32_16x16x32_bf16 v[42:45], v[170:173], v[206:209], v[42:45]
	v_mfma_f32_16x16x32_bf16 v[46:49], v[178:181], v[206:209], v[46:49]
	v_mfma_f32_16x16x32_bf16 v[22:25], v[170:173], v[214:217], v[22:25]
	v_mfma_f32_16x16x32_bf16 v[30:33], v[178:181], v[214:217], v[30:33]
	v_mfma_f32_16x16x32_bf16 v[10:13], v[170:173], v[222:225], v[10:13]
	v_mfma_f32_16x16x32_bf16 v[14:17], v[178:181], v[222:225], v[14:17]
	v_mfma_f32_16x16x32_bf16 v[54:57], v[174:177], v[202:205], v[54:57]
	v_mfma_f32_16x16x32_bf16 v[66:69], v[194:197], v[202:205], v[66:69]
	v_mfma_f32_16x16x32_bf16 v[42:45], v[174:177], v[210:213], v[42:45]
	v_mfma_f32_16x16x32_bf16 v[46:49], v[194:197], v[210:213], v[46:49]
	v_mfma_f32_16x16x32_bf16 v[22:25], v[174:177], v[218:221], v[22:25]
	v_mfma_f32_16x16x32_bf16 v[30:33], v[194:197], v[218:221], v[30:33]
	v_mfma_f32_16x16x32_bf16 v[10:13], v[174:177], v[226:229], v[10:13]
	v_mfma_f32_16x16x32_bf16 v[14:17], v[194:197], v[226:229], v[14:17]
	s_barrier
	s_setprio 0
	s_add_i32 s66, s66, 2
	s_add_u32 s52, s52, 0x10000
	s_addc_u32 s53, s53, 0
	s_add_u32 s49, s49, 0x10000
	s_addc_u32 s65, s65, 0
	s_cmpk_gt_u32 s66, 0x7d
	s_cbranch_scc0 .LBB0_1334
	s_and_b64 vcc, exec, s[10:11]
	s_cbranch_vccz .LBB0_1337
	s_barrier

.LBB0_1376:
	s_add_u32 s16, s44, 0x4000
	s_addc_u32 s17, s45, 0
	s_cmpk_eq_i32 s60, 0x7c
	s_cselect_b32 s48, s56, s16
	s_cselect_b32 s49, s11, s17
	s_cselect_b32 s47, s1, s59
	s_cselect_b32 s46, s57, s58
	s_add_u32 s42, s48, 0x8000
	s_addc_u32 s43, s49, 0
	s_add_i32 s16, 0, 0x10000
	v_add_u32_e32 v147, s16, v144
	s_add_i32 s61, 0, 0x14000
	ds_read_b128 v[148:151], v147
	ds_read_b128 v[152:155], v147 offset:1024
	ds_read_b128 v[158:161], v147 offset:2048
	ds_read_b128 v[166:169], v147 offset:3072
	v_add_u32_e32 v147, s61, v144
	ds_read_b128 v[170:173], v147
	ds_read_b128 v[174:177], v147 offset:1024
	ds_read_b128 v[178:181], v147 offset:2048
	ds_read_b128 v[194:197], v147 offset:3072
	v_lshl_add_u64 v[182:183], s[44:45], 0, v[114:115]
	s_add_i32 m0, s37, 0xc000
	ds_read_b128 v[198:201], v146
	ds_read_b128 v[202:205], v146 offset:1024
	ds_read_b128 v[206:209], v146 offset:2048
	ds_read_b128 v[210:213], v146 offset:3072
	ds_read_b128 v[214:217], v146 offset:4096
	ds_read_b128 v[218:221], v146 offset:5120
	ds_read_b128 v[222:225], v146 offset:6144
	ds_read_b128 v[226:229], v146 offset:7168
	global_load_lds_dwordx4 v[182:183], off
	v_lshl_add_u64 v[182:183], s[44:45], 0, v[142:143]
	s_add_i32 m0, s37, 0xe000
	s_nop 0
	global_load_lds_dwordx4 v[182:183], off
	s_waitcnt vmcnt(8)
	s_waitcnt lgkmcnt(0)
	s_setprio 1
	s_barrier
	v_mfma_f32_16x16x32_bf16 v[2:5], v[148:151], v[198:201], v[2:5]
	v_mfma_f32_16x16x32_bf16 v[6:9], v[158:161], v[198:201], v[6:9]
	v_mfma_f32_16x16x32_bf16 v[10:13], v[148:151], v[206:209], v[10:13]
	v_mfma_f32_16x16x32_bf16 v[14:17], v[158:161], v[206:209], v[14:17]
	v_mfma_f32_16x16x32_bf16 v[26:29], v[148:151], v[214:217], v[26:29]
	v_mfma_f32_16x16x32_bf16 v[30:33], v[158:161], v[214:217], v[30:33]
	v_mfma_f32_16x16x32_bf16 v[42:45], v[148:151], v[222:225], v[42:45]
	v_mfma_f32_16x16x32_bf16 v[46:49], v[158:161], v[222:225], v[46:49]
	v_mfma_f32_16x16x32_bf16 v[2:5], v[152:155], v[202:205], v[2:5]
	v_mfma_f32_16x16x32_bf16 v[6:9], v[166:169], v[202:205], v[6:9]
	v_mfma_f32_16x16x32_bf16 v[10:13], v[152:155], v[210:213], v[10:13]
	v_mfma_f32_16x16x32_bf16 v[14:17], v[166:169], v[210:213], v[14:17]
	v_mfma_f32_16x16x32_bf16 v[26:29], v[152:155], v[218:221], v[26:29]
	v_mfma_f32_16x16x32_bf16 v[30:33], v[166:169], v[218:221], v[30:33]
	v_mfma_f32_16x16x32_bf16 v[42:45], v[152:155], v[226:229], v[42:45]
	v_mfma_f32_16x16x32_bf16 v[46:49], v[166:169], v[226:229], v[46:49]
	s_setprio 0
	s_setprio 1
	v_mfma_f32_16x16x32_bf16 v[18:21], v[170:173], v[198:201], v[18:21]
	v_mfma_f32_16x16x32_bf16 v[22:25], v[178:181], v[198:201], v[22:25]
	v_mfma_f32_16x16x32_bf16 v[34:37], v[170:173], v[206:209], v[34:37]
	v_mfma_f32_16x16x32_bf16 v[38:41], v[178:181], v[206:209], v[38:41]
	v_mfma_f32_16x16x32_bf16 v[50:53], v[170:173], v[214:217], v[50:53]
	v_mfma_f32_16x16x32_bf16 v[54:57], v[178:181], v[214:217], v[54:57]
	v_mfma_f32_16x16x32_bf16 v[58:61], v[170:173], v[222:225], v[58:61]
	v_mfma_f32_16x16x32_bf16 v[62:65], v[178:181], v[222:225], v[62:65]
	v_mfma_f32_16x16x32_bf16 v[18:21], v[174:177], v[202:205], v[18:21]
	v_mfma_f32_16x16x32_bf16 v[22:25], v[194:197], v[202:205], v[22:25]
	v_mfma_f32_16x16x32_bf16 v[34:37], v[174:177], v[210:213], v[34:37]
	v_mfma_f32_16x16x32_bf16 v[38:41], v[194:197], v[210:213], v[38:41]
	v_mfma_f32_16x16x32_bf16 v[50:53], v[174:177], v[218:221], v[50:53]
	v_mfma_f32_16x16x32_bf16 v[54:57], v[194:197], v[218:221], v[54:57]
	v_mfma_f32_16x16x32_bf16 v[58:61], v[174:177], v[226:229], v[58:61]
	v_mfma_f32_16x16x32_bf16 v[62:65], v[194:197], v[226:229], v[62:65]
	s_barrier
	s_setprio 0
	s_add_i32 s16, s16, s24
	v_lshl_add_u64 v[182:183], s[46:47], 0, v[134:135]
	s_mov_b32 m0, s16
	ds_read_b128 v[198:201], v146 offset:16384
	ds_read_b128 v[202:205], v146 offset:17408
	ds_read_b128 v[206:209], v146 offset:18432
	ds_read_b128 v[210:213], v146 offset:19456
	ds_read_b128 v[214:217], v146 offset:20480
	ds_read_b128 v[218:221], v146 offset:21504
	ds_read_b128 v[222:225], v146 offset:22528
	ds_read_b128 v[226:229], v146 offset:23552
	global_load_lds_dwordx4 v[182:183], off
	s_add_i32 m0, s16, 0x2000
	s_add_u32 s16, s46, 0x1000
	v_lshl_add_u64 v[182:183], s[46:47], 0, v[138:139]
	s_addc_u32 s17, s47, 0
	s_add_i32 s61, s61, s24
	global_load_lds_dwordx4 v[182:183], off
	v_lshl_add_u64 v[182:183], s[16:17], 0, v[134:135]
	s_mov_b32 m0, s61
	s_nop 0
	global_load_lds_dwordx4 v[182:183], off
	v_lshl_add_u64 v[182:183], s[16:17], 0, v[138:139]
	s_add_i32 m0, s61, 0x2000
	s_nop 0
	global_load_lds_dwordx4 v[182:183], off
	v_lshl_add_u64 v[182:183], s[48:49], 0, v[132:133]
	s_mov_b32 m0, s37
	s_nop 0
	global_load_lds_dwordx4 v[182:183], off
	v_lshl_add_u64 v[182:183], s[48:49], 0, v[136:137]
	s_mov_b32 m0, s50
	s_nop 0
	global_load_lds_dwordx4 v[182:183], off
	s_waitcnt vmcnt(8)
	s_waitcnt lgkmcnt(0)
	s_setprio 1
	s_barrier
	v_mfma_f32_16x16x32_bf16 v[66:69], v[148:151], v[198:201], v[66:69]
	v_mfma_f32_16x16x32_bf16 v[70:73], v[158:161], v[198:201], v[70:73]
	v_mfma_f32_16x16x32_bf16 v[74:77], v[148:151], v[206:209], v[74:77]
	v_mfma_f32_16x16x32_bf16 v[78:81], v[158:161], v[206:209], v[78:81]
	v_mfma_f32_16x16x32_bf16 v[86:89], v[148:151], v[214:217], v[86:89]
	v_mfma_f32_16x16x32_bf16 v[94:97], v[158:161], v[214:217], v[94:97]
	v_mfma_f32_16x16x32_bf16 v[102:105], v[148:151], v[222:225], v[102:105]
	v_mfma_f32_16x16x32_bf16 v[110:113], v[158:161], v[222:225], v[110:113]
	v_mfma_f32_16x16x32_bf16 v[66:69], v[152:155], v[202:205], v[66:69]
	v_mfma_f32_16x16x32_bf16 v[70:73], v[166:169], v[202:205], v[70:73]
	v_mfma_f32_16x16x32_bf16 v[74:77], v[152:155], v[210:213], v[74:77]
	v_mfma_f32_16x16x32_bf16 v[78:81], v[166:169], v[210:213], v[78:81]
	v_mfma_f32_16x16x32_bf16 v[86:89], v[152:155], v[218:221], v[86:89]
	v_mfma_f32_16x16x32_bf16 v[94:97], v[166:169], v[218:221], v[94:97]
	v_mfma_f32_16x16x32_bf16 v[102:105], v[152:155], v[226:229], v[102:105]
	v_mfma_f32_16x16x32_bf16 v[110:113], v[166:169], v[226:229], v[110:113]
	s_setprio 0
	s_setprio 1
	v_mfma_f32_16x16x32_bf16 v[82:85], v[170:173], v[198:201], v[82:85]
	v_mfma_f32_16x16x32_bf16 v[90:93], v[178:181], v[198:201], v[90:93]
	v_mfma_f32_16x16x32_bf16 v[98:101], v[170:173], v[206:209], v[98:101]
	v_mfma_f32_16x16x32_bf16 v[106:109], v[178:181], v[206:209], v[106:109]
	v_mfma_f32_16x16x32_bf16 v[116:119], v[170:173], v[214:217], v[116:119]
	v_mfma_f32_16x16x32_bf16 v[120:123], v[178:181], v[214:217], v[120:123]
	v_mfma_f32_16x16x32_bf16 v[124:127], v[170:173], v[222:225], v[124:127]
	v_mfma_f32_16x16x32_bf16 v[128:131], v[178:181], v[222:225], v[128:131]
	v_mfma_f32_16x16x32_bf16 v[82:85], v[174:177], v[202:205], v[82:85]
	v_mfma_f32_16x16x32_bf16 v[90:93], v[194:197], v[202:205], v[90:93]
	v_mfma_f32_16x16x32_bf16 v[98:101], v[174:177], v[210:213], v[98:101]
	v_mfma_f32_16x16x32_bf16 v[106:109], v[194:197], v[210:213], v[106:109]
	v_mfma_f32_16x16x32_bf16 v[116:119], v[174:177], v[218:221], v[116:119]
	v_mfma_f32_16x16x32_bf16 v[120:123], v[194:197], v[218:221], v[120:123]
	v_mfma_f32_16x16x32_bf16 v[124:127], v[174:177], v[226:229], v[124:127]
	v_mfma_f32_16x16x32_bf16 v[128:131], v[194:197], v[226:229], v[128:131]
	s_barrier
	s_setprio 0
	s_add_i32 s61, 0, 0x18000
	v_add_u32_e32 v147, s61, v144
	s_add_i32 s62, 0, 0x1c000
	ds_read_b128 v[148:151], v147
	ds_read_b128 v[152:155], v147 offset:1024
	ds_read_b128 v[158:161], v147 offset:2048
	ds_read_b128 v[166:169], v147 offset:3072
	v_add_u32_e32 v147, s62, v144
	ds_read_b128 v[170:173], v147
	ds_read_b128 v[174:177], v147 offset:1024
	ds_read_b128 v[178:181], v147 offset:2048
	ds_read_b128 v[194:197], v147 offset:3072
	s_add_u32 s16, s48, 0x4000
	s_addc_u32 s17, s49, 0
	s_mov_b32 m0, s51
	v_lshl_add_u64 v[182:183], s[16:17], 0, v[132:133]
	ds_read_b128 v[198:201], v146 offset:32768
	ds_read_b128 v[202:205], v146 offset:33792
	ds_read_b128 v[206:209], v146 offset:34816
	ds_read_b128 v[210:213], v146 offset:35840
	ds_read_b128 v[214:217], v146 offset:36864
	ds_read_b128 v[218:221], v146 offset:37888
	ds_read_b128 v[222:225], v146 offset:38912
	ds_read_b128 v[226:229], v146 offset:39936
	global_load_lds_dwordx4 v[182:183], off
	v_lshl_add_u64 v[182:183], s[16:17], 0, v[136:137]
	s_mov_b32 m0, s52
	s_nop 0
	global_load_lds_dwordx4 v[182:183], off
	s_waitcnt vmcnt(8)
	s_waitcnt lgkmcnt(0)
	s_setprio 1
	s_barrier
	v_mfma_f32_16x16x32_bf16 v[2:5], v[148:151], v[198:201], v[2:5]
	v_mfma_f32_16x16x32_bf16 v[6:9], v[158:161], v[198:201], v[6:9]
	v_mfma_f32_16x16x32_bf16 v[10:13], v[148:151], v[206:209], v[10:13]
	v_mfma_f32_16x16x32_bf16 v[14:17], v[158:161], v[206:209], v[14:17]
	v_mfma_f32_16x16x32_bf16 v[26:29], v[148:151], v[214:217], v[26:29]
	v_mfma_f32_16x16x32_bf16 v[30:33], v[158:161], v[214:217], v[30:33]
	v_mfma_f32_16x16x32_bf16 v[42:45], v[148:151], v[222:225], v[42:45]
	v_mfma_f32_16x16x32_bf16 v[46:49], v[158:161], v[222:225], v[46:49]
	v_mfma_f32_16x16x32_bf16 v[2:5], v[152:155], v[202:205], v[2:5]
	v_mfma_f32_16x16x32_bf16 v[6:9], v[166:169], v[202:205], v[6:9]
	v_mfma_f32_16x16x32_bf16 v[10:13], v[152:155], v[210:213], v[10:13]
	v_mfma_f32_16x16x32_bf16 v[14:17], v[166:169], v[210:213], v[14:17]
	v_mfma_f32_16x16x32_bf16 v[26:29], v[152:155], v[218:221], v[26:29]
	v_mfma_f32_16x16x32_bf16 v[30:33], v[166:169], v[218:221], v[30:33]
	v_mfma_f32_16x16x32_bf16 v[42:45], v[152:155], v[226:229], v[42:45]
	v_mfma_f32_16x16x32_bf16 v[46:49], v[166:169], v[226:229], v[46:49]
	s_setprio 0
	s_setprio 1
	v_mfma_f32_16x16x32_bf16 v[18:21], v[170:173], v[198:201], v[18:21]
	v_mfma_f32_16x16x32_bf16 v[22:25], v[178:181], v[198:201], v[22:25]
	v_mfma_f32_16x16x32_bf16 v[34:37], v[170:173], v[206:209], v[34:37]
	v_mfma_f32_16x16x32_bf16 v[38:41], v[178:181], v[206:209], v[38:41]
	v_mfma_f32_16x16x32_bf16 v[50:53], v[170:173], v[214:217], v[50:53]
	v_mfma_f32_16x16x32_bf16 v[54:57], v[178:181], v[214:217], v[54:57]
	v_mfma_f32_16x16x32_bf16 v[58:61], v[170:173], v[222:225], v[58:61]
	v_mfma_f32_16x16x32_bf16 v[62:65], v[178:181], v[222:225], v[62:65]
	v_mfma_f32_16x16x32_bf16 v[18:21], v[174:177], v[202:205], v[18:21]
	v_mfma_f32_16x16x32_bf16 v[22:25], v[194:197], v[202:205], v[22:25]
	v_mfma_f32_16x16x32_bf16 v[34:37], v[174:177], v[210:213], v[34:37]
	v_mfma_f32_16x16x32_bf16 v[38:41], v[194:197], v[210:213], v[38:41]
	v_mfma_f32_16x16x32_bf16 v[50:53], v[174:177], v[218:221], v[50:53]
	v_mfma_f32_16x16x32_bf16 v[54:57], v[194:197], v[218:221], v[54:57]
	v_mfma_f32_16x16x32_bf16 v[58:61], v[174:177], v[226:229], v[58:61]
	v_mfma_f32_16x16x32_bf16 v[62:65], v[194:197], v[226:229], v[62:65]
	s_barrier
	s_setprio 0
	s_add_u32 s16, s46, 0x8000
	s_addc_u32 s17, s47, 0
	s_add_i32 s48, s61, s24
	v_lshl_add_u64 v[182:183], s[16:17], 0, v[134:135]
	s_mov_b32 m0, s48
	ds_read_b128 v[198:201], v146 offset:49152
	ds_read_b128 v[202:205], v146 offset:50176
	ds_read_b128 v[206:209], v146 offset:51200
	ds_read_b128 v[210:213], v146 offset:52224
	ds_read_b128 v[214:217], v146 offset:53248
	ds_read_b128 v[218:221], v146 offset:54272
	ds_read_b128 v[222:225], v146 offset:55296
	ds_read_b128 v[226:229], v146 offset:56320
	global_load_lds_dwordx4 v[182:183], off
	s_add_i32 m0, s48, 0x2000
	v_lshl_add_u64 v[182:183], s[16:17], 0, v[138:139]
	s_add_u32 s16, s46, 0x9000
	s_addc_u32 s17, s47, 0
	s_add_i32 s46, s62, s24
	global_load_lds_dwordx4 v[182:183], off
	v_lshl_add_u64 v[182:183], s[16:17], 0, v[134:135]
	s_mov_b32 m0, s46
	s_nop 0
	global_load_lds_dwordx4 v[182:183], off
	v_lshl_add_u64 v[182:183], s[16:17], 0, v[138:139]
	s_add_i32 m0, s46, 0x2000
	s_nop 0
	global_load_lds_dwordx4 v[182:183], off
	v_lshl_add_u64 v[182:183], s[42:43], 0, v[132:133]
	s_mov_b32 m0, s53
	s_nop 0
	global_load_lds_dwordx4 v[182:183], off
	v_lshl_add_u64 v[182:183], s[42:43], 0, v[136:137]
	s_mov_b32 m0, s54
	s_nop 0
	global_load_lds_dwordx4 v[182:183], off
	s_waitcnt vmcnt(8)
	s_waitcnt lgkmcnt(0)
	s_setprio 1
	s_barrier
	v_mfma_f32_16x16x32_bf16 v[66:69], v[148:151], v[198:201], v[66:69]
	v_mfma_f32_16x16x32_bf16 v[70:73], v[158:161], v[198:201], v[70:73]
	v_mfma_f32_16x16x32_bf16 v[74:77], v[148:151], v[206:209], v[74:77]
	v_mfma_f32_16x16x32_bf16 v[78:81], v[158:161], v[206:209], v[78:81]
	v_mfma_f32_16x16x32_bf16 v[86:89], v[148:151], v[214:217], v[86:89]
	v_mfma_f32_16x16x32_bf16 v[94:97], v[158:161], v[214:217], v[94:97]
	v_mfma_f32_16x16x32_bf16 v[102:105], v[148:151], v[222:225], v[102:105]
	v_mfma_f32_16x16x32_bf16 v[110:113], v[158:161], v[222:225], v[110:113]
	v_mfma_f32_16x16x32_bf16 v[66:69], v[152:155], v[202:205], v[66:69]
	v_mfma_f32_16x16x32_bf16 v[70:73], v[166:169], v[202:205], v[70:73]
	v_mfma_f32_16x16x32_bf16 v[74:77], v[152:155], v[210:213], v[74:77]
	v_mfma_f32_16x16x32_bf16 v[78:81], v[166:169], v[210:213], v[78:81]
	v_mfma_f32_16x16x32_bf16 v[86:89], v[152:155], v[218:221], v[86:89]
	v_mfma_f32_16x16x32_bf16 v[94:97], v[166:169], v[218:221], v[94:97]
	v_mfma_f32_16x16x32_bf16 v[102:105], v[152:155], v[226:229], v[102:105]
	v_mfma_f32_16x16x32_bf16 v[110:113], v[166:169], v[226:229], v[110:113]
	s_setprio 0
	s_setprio 1
	v_mfma_f32_16x16x32_bf16 v[82:85], v[170:173], v[198:201], v[82:85]
	v_mfma_f32_16x16x32_bf16 v[90:93], v[178:181], v[198:201], v[90:93]
	v_mfma_f32_16x16x32_bf16 v[98:101], v[170:173], v[206:209], v[98:101]
	v_mfma_f32_16x16x32_bf16 v[106:109], v[178:181], v[206:209], v[106:109]
	v_mfma_f32_16x16x32_bf16 v[116:119], v[170:173], v[214:217], v[116:119]
	v_mfma_f32_16x16x32_bf16 v[120:123], v[178:181], v[214:217], v[120:123]
	v_mfma_f32_16x16x32_bf16 v[124:127], v[170:173], v[222:225], v[124:127]
	v_mfma_f32_16x16x32_bf16 v[128:131], v[178:181], v[222:225], v[128:131]
	v_mfma_f32_16x16x32_bf16 v[82:85], v[174:177], v[202:205], v[82:85]
	v_mfma_f32_16x16x32_bf16 v[90:93], v[194:197], v[202:205], v[90:93]
	v_mfma_f32_16x16x32_bf16 v[98:101], v[174:177], v[210:213], v[98:101]
	v_mfma_f32_16x16x32_bf16 v[106:109], v[194:197], v[210:213], v[106:109]
	v_mfma_f32_16x16x32_bf16 v[116:119], v[174:177], v[218:221], v[116:119]
	v_mfma_f32_16x16x32_bf16 v[120:123], v[194:197], v[218:221], v[120:123]
	v_mfma_f32_16x16x32_bf16 v[124:127], v[174:177], v[226:229], v[124:127]
	v_mfma_f32_16x16x32_bf16 v[128:131], v[194:197], v[226:229], v[128:131]
	s_barrier
	s_setprio 0
	s_add_i32 s60, s60, 2
	s_add_u32 s44, s44, 0x10000
	s_addc_u32 s45, s45, 0
	s_add_u32 s58, s58, 0x10000
	s_addc_u32 s59, s59, 0
	s_cmpk_gt_u32 s60, 0x7d
	s_cbranch_scc0 .LBB0_1376
	s_and_b64 vcc, exec, s[8:9]
	s_cbranch_vccz .LBB0_1379
	s_barrier
